# epilogue bias waits of the fp8 GEMMs counted (vmcnt(8)) instead of draining the next unit's prefetched tiles; on top of w1 conversion in phase D
# speedup vs baseline: 1.0376x; 1.0055x over previous
.LBB0_255:
	v_mov_b32_e32 v2, v182
	s_nop 15
	s_nop 15
	s_lshl_b32 s19, s22, 8
	v_readfirstlane_b32 s17, v2
	s_ashr_i32 s22, s17, 2
	s_andn2_b32 s22, s22, 63
	s_lshr_b32 s17, s17, 1
	s_add_i32 s22, s22, s19
	s_lshl_b32 s19, s20, 8
	s_and_b32 s17, s17, 0x60
	v_and_or_b32 v16, v2, 15, s22
	s_or_b32 s17, s17, s19
	v_lshrrev_b32_e32 v2, 1, v2
	v_and_or_b32 v4, v2, 24, s17
	v_ashrrev_i32_e32 v5, 31, v4
	v_mov_b64_e32 v[2:3], s[8:9]
	v_mad_i64_i32 v[6:7], s[76:77], v16, s67, v[2:3]
	v_lshlrev_b64 v[4:5], 1, v[4:5]
	v_lshl_add_u64 v[10:11], v[6:7], 0, v[4:5]
	s_waitcnt vmcnt(8)
	v_pk_fma_f32 v[8:9], v[180:181], s[44:45], v[48:49] op_sel_hi:[1,0,1]
	v_pk_fma_f32 v[6:7], v[178:179], s[44:45], v[46:47] op_sel_hi:[1,0,1]
	v_pk_fma_f32 v[12:13], v[176:177], s[44:45], v[44:45] op_sel_hi:[1,0,1]
	v_pk_fma_f32 v[14:15], v[174:175], s[44:45], v[42:43] op_sel_hi:[1,0,1]
	v_cvt_pk_bf16_f32 v6, v6, v7
	v_cvt_pk_bf16_f32 v7, v8, v9
	v_cvt_pk_bf16_f32 v8, v14, v15
	v_cvt_pk_bf16_f32 v9, v12, v13
	global_store_dwordx4 v[10:11], v[6:9], off
	v_pk_fma_f32 v[12:13], v[160:161], s[44:45], v[36:37] op_sel_hi:[1,0,1]
	v_pk_fma_f32 v[14:15], v[158:159], s[44:45], v[34:35] op_sel_hi:[1,0,1]
	v_pk_fma_f32 v[8:9], v[168:169], s[44:45], v[40:41] op_sel_hi:[1,0,1]
	v_pk_fma_f32 v[6:7], v[166:167], s[44:45], v[38:39] op_sel_hi:[1,0,1]
	s_andn2_b64 vcc, exec, s[4:5]
	v_cvt_pk_bf16_f32 v6, v6, v7
	v_cvt_pk_bf16_f32 v7, v8, v9
	v_cvt_pk_bf16_f32 v8, v14, v15
	v_cvt_pk_bf16_f32 v9, v12, v13
	global_store_dwordx4 v[10:11], v[6:9], off offset:256
	v_pk_fma_f32 v[12:13], v[164:165], s[44:45], v[44:45] op_sel_hi:[1,0,1]
	v_pk_fma_f32 v[14:15], v[162:163], s[44:45], v[42:43] op_sel_hi:[1,0,1]
	v_or_b32_e32 v6, 16, v16
	v_mad_i64_i32 v[6:7], s[76:77], v6, s67, v[2:3]
	v_lshl_add_u64 v[10:11], v[6:7], 0, v[4:5]
	v_pk_fma_f32 v[8:9], v[172:173], s[44:45], v[48:49] op_sel_hi:[1,0,1]
	v_pk_fma_f32 v[6:7], v[170:171], s[44:45], v[46:47] op_sel_hi:[1,0,1]
	s_mov_b64 s[4:5], -1
	v_cvt_pk_bf16_f32 v6, v6, v7
	v_cvt_pk_bf16_f32 v7, v8, v9
	v_cvt_pk_bf16_f32 v8, v14, v15
	v_cvt_pk_bf16_f32 v9, v12, v13
	global_store_dwordx4 v[10:11], v[6:9], off
	v_pk_fma_f32 v[12:13], v[144:145], s[44:45], v[36:37] op_sel_hi:[1,0,1]
	v_pk_fma_f32 v[14:15], v[142:143], s[44:45], v[34:35] op_sel_hi:[1,0,1]
	v_pk_fma_f32 v[8:9], v[152:153], s[44:45], v[40:41] op_sel_hi:[1,0,1]
	v_pk_fma_f32 v[6:7], v[150:151], s[44:45], v[38:39] op_sel_hi:[1,0,1]
	s_nop 0
	v_cvt_pk_bf16_f32 v6, v6, v7
	v_cvt_pk_bf16_f32 v7, v8, v9
	v_cvt_pk_bf16_f32 v8, v14, v15
	v_cvt_pk_bf16_f32 v9, v12, v13
	global_store_dwordx4 v[10:11], v[6:9], off offset:256
	v_pk_fma_f32 v[12:13], v[148:149], s[44:45], v[44:45] op_sel_hi:[1,0,1]
	v_pk_fma_f32 v[14:15], v[146:147], s[44:45], v[42:43] op_sel_hi:[1,0,1]
	v_or_b32_e32 v6, 32, v16
	v_mad_i64_i32 v[6:7], s[76:77], v6, s67, v[2:3]
	v_lshl_add_u64 v[10:11], v[6:7], 0, v[4:5]
	v_pk_fma_f32 v[8:9], v[156:157], s[44:45], v[48:49] op_sel_hi:[1,0,1]
	v_pk_fma_f32 v[6:7], v[154:155], s[44:45], v[46:47] op_sel_hi:[1,0,1]
	s_nop 0
	v_cvt_pk_bf16_f32 v6, v6, v7
	v_cvt_pk_bf16_f32 v7, v8, v9
	v_cvt_pk_bf16_f32 v8, v14, v15
	v_cvt_pk_bf16_f32 v9, v12, v13
	global_store_dwordx4 v[10:11], v[6:9], off
	v_pk_fma_f32 v[12:13], v[128:129], s[44:45], v[36:37] op_sel_hi:[1,0,1]
	v_pk_fma_f32 v[14:15], v[126:127], s[44:45], v[34:35] op_sel_hi:[1,0,1]
	v_pk_fma_f32 v[8:9], v[136:137], s[44:45], v[40:41] op_sel_hi:[1,0,1]
	v_pk_fma_f32 v[6:7], v[134:135], s[44:45], v[38:39] op_sel_hi:[1,0,1]
	s_nop 0
	v_cvt_pk_bf16_f32 v6, v6, v7
	v_cvt_pk_bf16_f32 v7, v8, v9
	v_cvt_pk_bf16_f32 v8, v14, v15
	v_cvt_pk_bf16_f32 v9, v12, v13
	global_store_dwordx4 v[10:11], v[6:9], off offset:256
	v_pk_fma_f32 v[12:13], v[132:133], s[44:45], v[44:45] op_sel_hi:[1,0,1]
	v_pk_fma_f32 v[14:15], v[130:131], s[44:45], v[42:43] op_sel_hi:[1,0,1]
	v_or_b32_e32 v6, 48, v16
	v_mad_i64_i32 v[6:7], s[76:77], v6, s67, v[2:3]
	v_lshl_add_u64 v[10:11], v[6:7], 0, v[4:5]
	v_pk_fma_f32 v[8:9], v[140:141], s[44:45], v[48:49] op_sel_hi:[1,0,1]
	v_pk_fma_f32 v[6:7], v[138:139], s[44:45], v[46:47] op_sel_hi:[1,0,1]
	s_nop 0
	v_cvt_pk_bf16_f32 v6, v6, v7
	v_cvt_pk_bf16_f32 v7, v8, v9
	v_cvt_pk_bf16_f32 v8, v14, v15
	v_cvt_pk_bf16_f32 v9, v12, v13
	global_store_dwordx4 v[10:11], v[6:9], off
	v_pk_fma_f32 v[12:13], v[120:121], s[44:45], v[36:37] op_sel_hi:[1,0,1]
	v_pk_fma_f32 v[14:15], v[118:119], s[44:45], v[34:35] op_sel_hi:[1,0,1]
	v_pk_fma_f32 v[8:9], v[124:125], s[44:45], v[40:41] op_sel_hi:[1,0,1]
	v_pk_fma_f32 v[6:7], v[122:123], s[44:45], v[38:39] op_sel_hi:[1,0,1]
	s_nop 0
	v_cvt_pk_bf16_f32 v6, v6, v7
	v_cvt_pk_bf16_f32 v7, v8, v9
	v_cvt_pk_bf16_f32 v8, v14, v15
	v_cvt_pk_bf16_f32 v9, v12, v13
	global_store_dwordx4 v[10:11], v[6:9], off offset:256
	v_pk_fma_f32 v[12:13], v[112:113], s[44:45], v[44:45] op_sel_hi:[1,0,1]
	v_pk_fma_f32 v[14:15], v[110:111], s[44:45], v[42:43] op_sel_hi:[1,0,1]
	v_add_u32_e32 v6, 0x80, v16
	v_mad_i64_i32 v[6:7], s[76:77], v6, s67, v[2:3]
	v_lshl_add_u64 v[10:11], v[6:7], 0, v[4:5]
	v_pk_fma_f32 v[8:9], v[116:117], s[44:45], v[48:49] op_sel_hi:[1,0,1]
	v_pk_fma_f32 v[6:7], v[114:115], s[44:45], v[46:47] op_sel_hi:[1,0,1]
	s_nop 0
	v_cvt_pk_bf16_f32 v6, v6, v7
	v_cvt_pk_bf16_f32 v7, v8, v9
	v_cvt_pk_bf16_f32 v8, v14, v15
	v_cvt_pk_bf16_f32 v9, v12, v13
	global_store_dwordx4 v[10:11], v[6:9], off
	v_pk_fma_f32 v[12:13], v[96:97], s[44:45], v[36:37] op_sel_hi:[1,0,1]
	v_pk_fma_f32 v[14:15], v[94:95], s[44:45], v[34:35] op_sel_hi:[1,0,1]
	v_pk_fma_f32 v[8:9], v[104:105], s[44:45], v[40:41] op_sel_hi:[1,0,1]
	v_pk_fma_f32 v[6:7], v[102:103], s[44:45], v[38:39] op_sel_hi:[1,0,1]
	s_nop 0
	v_cvt_pk_bf16_f32 v6, v6, v7
	v_cvt_pk_bf16_f32 v7, v8, v9
	v_cvt_pk_bf16_f32 v8, v14, v15
	v_cvt_pk_bf16_f32 v9, v12, v13
	global_store_dwordx4 v[10:11], v[6:9], off offset:256
	v_pk_fma_f32 v[12:13], v[100:101], s[44:45], v[44:45] op_sel_hi:[1,0,1]
	v_pk_fma_f32 v[14:15], v[98:99], s[44:45], v[42:43] op_sel_hi:[1,0,1]
	v_add_u32_e32 v6, 0x90, v16
	v_mad_i64_i32 v[6:7], s[76:77], v6, s67, v[2:3]
	v_lshl_add_u64 v[10:11], v[6:7], 0, v[4:5]
	v_pk_fma_f32 v[8:9], v[108:109], s[44:45], v[48:49] op_sel_hi:[1,0,1]
	v_pk_fma_f32 v[6:7], v[106:107], s[44:45], v[46:47] op_sel_hi:[1,0,1]
	s_nop 0
	v_cvt_pk_bf16_f32 v6, v6, v7
	v_cvt_pk_bf16_f32 v7, v8, v9
	v_cvt_pk_bf16_f32 v8, v14, v15
	v_cvt_pk_bf16_f32 v9, v12, v13
	global_store_dwordx4 v[10:11], v[6:9], off
	v_pk_fma_f32 v[12:13], v[80:81], s[44:45], v[36:37] op_sel_hi:[1,0,1]
	v_pk_fma_f32 v[14:15], v[78:79], s[44:45], v[34:35] op_sel_hi:[1,0,1]
	v_pk_fma_f32 v[8:9], v[88:89], s[44:45], v[40:41] op_sel_hi:[1,0,1]
	v_pk_fma_f32 v[6:7], v[86:87], s[44:45], v[38:39] op_sel_hi:[1,0,1]
	s_nop 0
	v_cvt_pk_bf16_f32 v6, v6, v7
	v_cvt_pk_bf16_f32 v7, v8, v9
	v_cvt_pk_bf16_f32 v8, v14, v15
	v_cvt_pk_bf16_f32 v9, v12, v13
	global_store_dwordx4 v[10:11], v[6:9], off offset:256
	v_pk_fma_f32 v[12:13], v[84:85], s[44:45], v[44:45] op_sel_hi:[1,0,1]
	v_pk_fma_f32 v[14:15], v[82:83], s[44:45], v[42:43] op_sel_hi:[1,0,1]
	v_add_u32_e32 v6, 0xa0, v16
	v_mad_i64_i32 v[6:7], s[76:77], v6, s67, v[2:3]
	v_lshl_add_u64 v[10:11], v[6:7], 0, v[4:5]
	v_pk_fma_f32 v[8:9], v[92:93], s[44:45], v[48:49] op_sel_hi:[1,0,1]
	v_pk_fma_f32 v[6:7], v[90:91], s[44:45], v[46:47] op_sel_hi:[1,0,1]
	s_nop 0
	v_cvt_pk_bf16_f32 v6, v6, v7
	v_cvt_pk_bf16_f32 v7, v8, v9
	v_cvt_pk_bf16_f32 v8, v14, v15
	v_cvt_pk_bf16_f32 v9, v12, v13
	global_store_dwordx4 v[10:11], v[6:9], off
	v_pk_fma_f32 v[12:13], v[60:61], s[44:45], v[36:37] op_sel_hi:[1,0,1]
	v_pk_fma_f32 v[14:15], v[58:59], s[44:45], v[34:35] op_sel_hi:[1,0,1]
	v_pk_fma_f32 v[8:9], v[72:73], s[44:45], v[40:41] op_sel_hi:[1,0,1]
	v_pk_fma_f32 v[6:7], v[70:71], s[44:45], v[38:39] op_sel_hi:[1,0,1]
	s_nop 0
	v_cvt_pk_bf16_f32 v6, v6, v7
	v_cvt_pk_bf16_f32 v7, v8, v9
	v_cvt_pk_bf16_f32 v8, v14, v15
	v_cvt_pk_bf16_f32 v9, v12, v13
	global_store_dwordx4 v[10:11], v[6:9], off offset:256
	v_pk_fma_f32 v[10:11], v[62:63], s[44:45], v[42:43] op_sel_hi:[1,0,1]
	s_nop 0
	v_add_u32_e32 v6, 0xb0, v16
	v_mad_i64_i32 v[2:3], s[76:77], v6, s67, v[2:3]
	v_lshl_add_u64 v[6:7], v[2:3], 0, v[4:5]
	v_pk_fma_f32 v[4:5], v[76:77], s[44:45], v[48:49] op_sel_hi:[1,0,1]
	v_pk_fma_f32 v[2:3], v[74:75], s[44:45], v[46:47] op_sel_hi:[1,0,1]
	v_pk_fma_f32 v[8:9], v[64:65], s[44:45], v[44:45] op_sel_hi:[1,0,1]
	v_cvt_pk_bf16_f32 v2, v2, v3
	v_cvt_pk_bf16_f32 v3, v4, v5
	v_cvt_pk_bf16_f32 v4, v10, v11
	v_cvt_pk_bf16_f32 v5, v8, v9
	global_store_dwordx4 v[6:7], v[2:5], off
	v_pk_fma_f32 v[8:9], v[52:53], s[44:45], v[36:37] op_sel_hi:[1,0,1]
	v_pk_fma_f32 v[10:11], v[50:51], s[44:45], v[34:35] op_sel_hi:[1,0,1]
	v_pk_fma_f32 v[4:5], v[56:57], s[44:45], v[40:41] op_sel_hi:[1,0,1]
	v_pk_fma_f32 v[2:3], v[54:55], s[44:45], v[38:39] op_sel_hi:[1,0,1]
	s_nop 0
	v_cvt_pk_bf16_f32 v2, v2, v3
	v_cvt_pk_bf16_f32 v3, v4, v5
	v_cvt_pk_bf16_f32 v4, v10, v11
	v_cvt_pk_bf16_f32 v5, v8, v9
	global_store_dwordx4 v[6:7], v[2:5], off offset:256
	s_cbranch_vccnz .LBB0_248
	s_nop 0
	v_lshl_or_b32 v2, s18, 8, v205
	v_ashrrev_i32_e32 v3, 31, v2
	v_lshl_add_u64 v[2:3], v[2:3], 2, s[10:11]
	global_load_dwordx4 v[42:45], v[2:3], off offset:16
	global_load_dwordx4 v[46:49], v[2:3], off
	global_load_dwordx4 v[34:37], v[2:3], off offset:528
	global_load_dwordx4 v[38:41], v[2:3], off offset:512
	s_andn2_b64 vcc, exec, s[12:13]
	s_cbranch_vccnz .LBB0_247
	s_barrier
	s_branch .LBB0_247

.LBB0_271:
	v_mov_b32_e32 v2, v182
	s_nop 15
	s_nop 15
	s_lshl_b32 s22, s77, 2
	v_readfirstlane_b32 s20, v2
	v_lshrrev_b32_e32 v3, 1, v2
	s_lshr_b32 s21, s20, 2
	s_bfe_u32 s23, s20, 0x10007
	s_lshr_b32 s20, s20, 1
	v_and_b32_e32 v3, 24, v3
	v_and_or_b32 v12, s20, 32, v3
	s_lshl_b32 s20, s77, 3
	s_and_b32 s21, s21, 0x1ffffc0
	s_and_b32 s20, s20, 0x1ffff00
	s_and_b32 s22, s22, 0x7c
	s_add_i32 s21, s21, s20
	s_or_b32 s22, s23, s22
	v_and_or_b32 v2, v2, 15, s21
	v_lshl_or_b32 v2, v2, 7, s22
	s_waitcnt vmcnt(8)
	v_pk_fma_f32 v[6:7], v[164:165], s[50:51], v[180:181] op_sel_hi:[1,0,0]
	v_pk_fma_f32 v[4:5], v[162:163], s[50:51], v[180:181] op_sel_hi:[1,0,0]
	v_pk_fma_f32 v[8:9], v[160:161], s[50:51], v[180:181] op_sel_hi:[1,0,0]
	v_ashrrev_i32_e32 v3, 31, v2
	v_cvt_pk_bf16_f32 v4, v4, v5
	v_cvt_pk_bf16_f32 v5, v6, v7
	v_cvt_pk_bf16_f32 v7, v8, v9
	v_lshlrev_b64 v[8:9], 8, v[2:3]
	s_lshl_b32 s40, s40, 7
	v_lshl_add_u64 v[8:9], s[10:11], 0, v[8:9]
	v_pk_fma_f32 v[10:11], v[158:159], s[50:51], v[180:181] op_sel_hi:[1,0,0]
	v_lshl_add_u64 v[8:9], v[8:9], 0, s[40:41]
	v_lshlrev_b32_e32 v214, 1, v12
	v_cvt_pk_bf16_f32 v6, v10, v11
	v_lshl_add_u64 v[8:9], v[8:9], 0, v[214:215]
	global_store_dwordx4 v[8:9], v[4:7], off
	v_pk_fma_f32 v[8:9], v[148:149], s[50:51], v[180:181] op_sel_hi:[1,0,0]
	v_pk_fma_f32 v[10:11], v[146:147], s[50:51], v[180:181] op_sel_hi:[1,0,0]
	v_pk_fma_f32 v[6:7], v[156:157], s[50:51], v[180:181] op_sel_hi:[1,0,0]
	v_pk_fma_f32 v[4:5], v[154:155], s[50:51], v[180:181] op_sel_hi:[1,0,0]
	v_pk_fma_f32 v[12:13], v[142:143], s[50:51], v[178:179] op_sel_hi:[1,0,0]
	v_cvt_pk_bf16_f32 v4, v4, v5
	v_cvt_pk_bf16_f32 v5, v6, v7
	v_cvt_pk_bf16_f32 v7, v8, v9
	v_or_b32_e32 v8, 2, v2
	v_ashrrev_i32_e32 v9, 31, v8
	v_lshlrev_b64 v[8:9], 8, v[8:9]
	v_lshl_add_u64 v[8:9], s[10:11], 0, v[8:9]
	v_lshl_add_u64 v[8:9], v[8:9], 0, s[40:41]
	v_cvt_pk_bf16_f32 v6, v10, v11
	v_lshl_add_u64 v[8:9], v[8:9], 0, v[214:215]
	global_store_dwordx4 v[8:9], v[4:7], off
	v_or_b32_e32 v8, 0x800, v2
	v_ashrrev_i32_e32 v9, 31, v8
	v_lshlrev_b64 v[8:9], 8, v[8:9]
	v_lshl_add_u64 v[8:9], s[10:11], 0, v[8:9]
	v_pk_fma_f32 v[6:7], v[152:153], s[50:51], v[178:179] op_sel_hi:[1,0,0]
	v_pk_fma_f32 v[4:5], v[150:151], s[50:51], v[178:179] op_sel_hi:[1,0,0]
	v_pk_fma_f32 v[10:11], v[144:145], s[50:51], v[178:179] op_sel_hi:[1,0,0]
	v_lshl_add_u64 v[8:9], v[8:9], 0, s[40:41]
	v_cvt_pk_bf16_f32 v4, v4, v5
	v_cvt_pk_bf16_f32 v5, v6, v7
	v_cvt_pk_bf16_f32 v6, v12, v13
	v_cvt_pk_bf16_f32 v7, v10, v11
	v_lshl_add_u64 v[8:9], v[8:9], 0, v[214:215]
	global_store_dwordx4 v[8:9], v[4:7], off
	v_pk_fma_f32 v[8:9], v[132:133], s[50:51], v[178:179] op_sel_hi:[1,0,0]
	v_pk_fma_f32 v[10:11], v[130:131], s[50:51], v[178:179] op_sel_hi:[1,0,0]
	v_pk_fma_f32 v[6:7], v[140:141], s[50:51], v[178:179] op_sel_hi:[1,0,0]
	v_pk_fma_f32 v[4:5], v[138:139], s[50:51], v[178:179] op_sel_hi:[1,0,0]
	v_pk_fma_f32 v[12:13], v[126:127], s[50:51], v[176:177] op_sel_hi:[1,0,0]
	v_cvt_pk_bf16_f32 v4, v4, v5
	v_cvt_pk_bf16_f32 v5, v6, v7
	v_cvt_pk_bf16_f32 v7, v8, v9
	v_or_b32_e32 v8, 0x802, v2
	v_ashrrev_i32_e32 v9, 31, v8
	v_lshlrev_b64 v[8:9], 8, v[8:9]
	v_lshl_add_u64 v[8:9], s[10:11], 0, v[8:9]
	v_lshl_add_u64 v[8:9], v[8:9], 0, s[40:41]
	v_cvt_pk_bf16_f32 v6, v10, v11
	v_lshl_add_u64 v[8:9], v[8:9], 0, v[214:215]
	global_store_dwordx4 v[8:9], v[4:7], off
	v_or_b32_e32 v8, 0x1000, v2
	v_ashrrev_i32_e32 v9, 31, v8
	v_lshlrev_b64 v[8:9], 8, v[8:9]
	v_lshl_add_u64 v[8:9], s[10:11], 0, v[8:9]
	v_pk_fma_f32 v[6:7], v[136:137], s[50:51], v[176:177] op_sel_hi:[1,0,0]
	v_pk_fma_f32 v[4:5], v[134:135], s[50:51], v[176:177] op_sel_hi:[1,0,0]
	v_pk_fma_f32 v[10:11], v[128:129], s[50:51], v[176:177] op_sel_hi:[1,0,0]
	v_lshl_add_u64 v[8:9], v[8:9], 0, s[40:41]
	v_cvt_pk_bf16_f32 v4, v4, v5
	v_cvt_pk_bf16_f32 v5, v6, v7
	v_cvt_pk_bf16_f32 v6, v12, v13
	v_cvt_pk_bf16_f32 v7, v10, v11
	v_lshl_add_u64 v[8:9], v[8:9], 0, v[214:215]
	global_store_dwordx4 v[8:9], v[4:7], off
	v_pk_fma_f32 v[8:9], v[116:117], s[50:51], v[176:177] op_sel_hi:[1,0,0]
	v_pk_fma_f32 v[10:11], v[114:115], s[50:51], v[176:177] op_sel_hi:[1,0,0]
	v_pk_fma_f32 v[6:7], v[124:125], s[50:51], v[176:177] op_sel_hi:[1,0,0]
	v_pk_fma_f32 v[4:5], v[122:123], s[50:51], v[176:177] op_sel_hi:[1,0,0]
	v_pk_fma_f32 v[12:13], v[110:111], s[50:51], v[174:175] op_sel_hi:[1,0,0]
	v_cvt_pk_bf16_f32 v4, v4, v5
	v_cvt_pk_bf16_f32 v5, v6, v7
	v_cvt_pk_bf16_f32 v7, v8, v9
	v_or_b32_e32 v8, 0x1002, v2
	v_ashrrev_i32_e32 v9, 31, v8
	v_lshlrev_b64 v[8:9], 8, v[8:9]
	v_lshl_add_u64 v[8:9], s[10:11], 0, v[8:9]
	v_lshl_add_u64 v[8:9], v[8:9], 0, s[40:41]
	v_cvt_pk_bf16_f32 v6, v10, v11
	v_lshl_add_u64 v[8:9], v[8:9], 0, v[214:215]
	global_store_dwordx4 v[8:9], v[4:7], off
	v_or_b32_e32 v8, 0x1800, v2
	v_ashrrev_i32_e32 v9, 31, v8
	v_lshlrev_b64 v[8:9], 8, v[8:9]
	v_lshl_add_u64 v[8:9], s[10:11], 0, v[8:9]
	v_pk_fma_f32 v[6:7], v[120:121], s[50:51], v[174:175] op_sel_hi:[1,0,0]
	v_pk_fma_f32 v[4:5], v[118:119], s[50:51], v[174:175] op_sel_hi:[1,0,0]
	v_pk_fma_f32 v[10:11], v[112:113], s[50:51], v[174:175] op_sel_hi:[1,0,0]
	v_lshl_add_u64 v[8:9], v[8:9], 0, s[40:41]
	v_cvt_pk_bf16_f32 v4, v4, v5
	v_cvt_pk_bf16_f32 v5, v6, v7
	v_cvt_pk_bf16_f32 v6, v12, v13
	v_cvt_pk_bf16_f32 v7, v10, v11
	v_lshl_add_u64 v[8:9], v[8:9], 0, v[214:215]
	global_store_dwordx4 v[8:9], v[4:7], off
	v_pk_fma_f32 v[8:9], v[104:105], s[50:51], v[174:175] op_sel_hi:[1,0,0]
	v_pk_fma_f32 v[10:11], v[102:103], s[50:51], v[174:175] op_sel_hi:[1,0,0]
	v_pk_fma_f32 v[6:7], v[108:109], s[50:51], v[174:175] op_sel_hi:[1,0,0]
	v_pk_fma_f32 v[4:5], v[106:107], s[50:51], v[174:175] op_sel_hi:[1,0,0]
	v_pk_fma_f32 v[12:13], v[94:95], s[50:51], v[172:173] op_sel_hi:[1,0,0]
	v_cvt_pk_bf16_f32 v4, v4, v5
	v_cvt_pk_bf16_f32 v5, v6, v7
	v_cvt_pk_bf16_f32 v7, v8, v9
	v_or_b32_e32 v8, 0x1802, v2
	v_ashrrev_i32_e32 v9, 31, v8
	v_lshlrev_b64 v[8:9], 8, v[8:9]
	v_lshl_add_u64 v[8:9], s[10:11], 0, v[8:9]
	v_lshl_add_u64 v[8:9], v[8:9], 0, s[40:41]
	v_cvt_pk_bf16_f32 v6, v10, v11
	v_lshl_add_u64 v[8:9], v[8:9], 0, v[214:215]
	global_store_dwordx4 v[8:9], v[4:7], off
	v_add_u32_e32 v8, 0x4000, v2
	v_ashrrev_i32_e32 v9, 31, v8
	v_lshlrev_b64 v[8:9], 8, v[8:9]
	v_lshl_add_u64 v[8:9], s[10:11], 0, v[8:9]
	v_pk_fma_f32 v[6:7], v[100:101], s[50:51], v[172:173] op_sel_hi:[1,0,0]
	v_pk_fma_f32 v[4:5], v[98:99], s[50:51], v[172:173] op_sel_hi:[1,0,0]
	v_pk_fma_f32 v[10:11], v[96:97], s[50:51], v[172:173] op_sel_hi:[1,0,0]
	v_lshl_add_u64 v[8:9], v[8:9], 0, s[40:41]
	v_cvt_pk_bf16_f32 v4, v4, v5
	v_cvt_pk_bf16_f32 v5, v6, v7
	v_cvt_pk_bf16_f32 v6, v12, v13
	v_cvt_pk_bf16_f32 v7, v10, v11
	v_lshl_add_u64 v[8:9], v[8:9], 0, v[214:215]
	global_store_dwordx4 v[8:9], v[4:7], off
	v_pk_fma_f32 v[8:9], v[84:85], s[50:51], v[172:173] op_sel_hi:[1,0,0]
	v_pk_fma_f32 v[10:11], v[82:83], s[50:51], v[172:173] op_sel_hi:[1,0,0]
	v_pk_fma_f32 v[6:7], v[92:93], s[50:51], v[172:173] op_sel_hi:[1,0,0]
	v_pk_fma_f32 v[4:5], v[90:91], s[50:51], v[172:173] op_sel_hi:[1,0,0]
	v_pk_fma_f32 v[12:13], v[78:79], s[50:51], v[170:171] op_sel_hi:[1,0,0]
	v_cvt_pk_bf16_f32 v4, v4, v5
	v_cvt_pk_bf16_f32 v5, v6, v7
	v_cvt_pk_bf16_f32 v7, v8, v9
	v_add_u32_e32 v8, 0x4002, v2
	v_ashrrev_i32_e32 v9, 31, v8
	v_lshlrev_b64 v[8:9], 8, v[8:9]
	v_lshl_add_u64 v[8:9], s[10:11], 0, v[8:9]
	v_lshl_add_u64 v[8:9], v[8:9], 0, s[40:41]
	v_cvt_pk_bf16_f32 v6, v10, v11
	v_lshl_add_u64 v[8:9], v[8:9], 0, v[214:215]
	global_store_dwordx4 v[8:9], v[4:7], off
	v_add_u32_e32 v8, 0x4800, v2
	v_ashrrev_i32_e32 v9, 31, v8
	v_lshlrev_b64 v[8:9], 8, v[8:9]
	v_lshl_add_u64 v[8:9], s[10:11], 0, v[8:9]
	v_pk_fma_f32 v[6:7], v[88:89], s[50:51], v[170:171] op_sel_hi:[1,0,0]
	v_pk_fma_f32 v[4:5], v[86:87], s[50:51], v[170:171] op_sel_hi:[1,0,0]
	v_pk_fma_f32 v[10:11], v[80:81], s[50:51], v[170:171] op_sel_hi:[1,0,0]
	v_lshl_add_u64 v[8:9], v[8:9], 0, s[40:41]
	v_cvt_pk_bf16_f32 v4, v4, v5
	v_cvt_pk_bf16_f32 v5, v6, v7
	v_cvt_pk_bf16_f32 v6, v12, v13
	v_cvt_pk_bf16_f32 v7, v10, v11
	v_lshl_add_u64 v[8:9], v[8:9], 0, v[214:215]
	global_store_dwordx4 v[8:9], v[4:7], off
	v_pk_fma_f32 v[8:9], v[64:65], s[50:51], v[170:171] op_sel_hi:[1,0,0]
	v_pk_fma_f32 v[10:11], v[62:63], s[50:51], v[170:171] op_sel_hi:[1,0,0]
	v_pk_fma_f32 v[6:7], v[76:77], s[50:51], v[170:171] op_sel_hi:[1,0,0]
	v_pk_fma_f32 v[4:5], v[74:75], s[50:51], v[170:171] op_sel_hi:[1,0,0]
	v_pk_fma_f32 v[12:13], v[58:59], s[50:51], v[168:169] op_sel_hi:[1,0,0]
	v_cvt_pk_bf16_f32 v4, v4, v5
	v_cvt_pk_bf16_f32 v5, v6, v7
	v_cvt_pk_bf16_f32 v7, v8, v9
	v_add_u32_e32 v8, 0x4802, v2
	v_ashrrev_i32_e32 v9, 31, v8
	v_lshlrev_b64 v[8:9], 8, v[8:9]
	v_lshl_add_u64 v[8:9], s[10:11], 0, v[8:9]
	v_lshl_add_u64 v[8:9], v[8:9], 0, s[40:41]
	v_cvt_pk_bf16_f32 v6, v10, v11
	v_lshl_add_u64 v[8:9], v[8:9], 0, v[214:215]
	global_store_dwordx4 v[8:9], v[4:7], off
	v_add_u32_e32 v8, 0x5000, v2
	v_ashrrev_i32_e32 v9, 31, v8
	v_lshlrev_b64 v[8:9], 8, v[8:9]
	v_lshl_add_u64 v[8:9], s[10:11], 0, v[8:9]
	v_pk_fma_f32 v[6:7], v[72:73], s[50:51], v[168:169] op_sel_hi:[1,0,0]
	v_pk_fma_f32 v[4:5], v[70:71], s[50:51], v[168:169] op_sel_hi:[1,0,0]
	v_pk_fma_f32 v[10:11], v[60:61], s[50:51], v[168:169] op_sel_hi:[1,0,0]
	v_lshl_add_u64 v[8:9], v[8:9], 0, s[40:41]
	v_cvt_pk_bf16_f32 v4, v4, v5
	v_cvt_pk_bf16_f32 v5, v6, v7
	v_cvt_pk_bf16_f32 v6, v12, v13
	v_cvt_pk_bf16_f32 v7, v10, v11
	v_lshl_add_u64 v[8:9], v[8:9], 0, v[214:215]
	global_store_dwordx4 v[8:9], v[4:7], off
	v_pk_fma_f32 v[8:9], v[48:49], s[50:51], v[168:169] op_sel_hi:[1,0,0]
	v_pk_fma_f32 v[10:11], v[46:47], s[50:51], v[168:169] op_sel_hi:[1,0,0]
	v_pk_fma_f32 v[6:7], v[56:57], s[50:51], v[168:169] op_sel_hi:[1,0,0]
	v_pk_fma_f32 v[4:5], v[54:55], s[50:51], v[168:169] op_sel_hi:[1,0,0]
	v_pk_fma_f32 v[12:13], v[42:43], s[50:51], v[166:167] op_sel_hi:[1,0,0]
	v_cvt_pk_bf16_f32 v4, v4, v5
	v_cvt_pk_bf16_f32 v5, v6, v7
	v_cvt_pk_bf16_f32 v7, v8, v9
	v_add_u32_e32 v8, 0x5002, v2
	v_ashrrev_i32_e32 v9, 31, v8
	v_lshlrev_b64 v[8:9], 8, v[8:9]
	v_lshl_add_u64 v[8:9], s[10:11], 0, v[8:9]
	v_lshl_add_u64 v[8:9], v[8:9], 0, s[40:41]
	v_cvt_pk_bf16_f32 v6, v10, v11
	v_lshl_add_u64 v[8:9], v[8:9], 0, v[214:215]
	global_store_dwordx4 v[8:9], v[4:7], off
	v_add_u32_e32 v8, 0x5800, v2
	v_ashrrev_i32_e32 v9, 31, v8
	v_lshlrev_b64 v[8:9], 8, v[8:9]
	v_add_u32_e32 v2, 0x5802, v2
	v_lshl_add_u64 v[8:9], s[10:11], 0, v[8:9]
	v_ashrrev_i32_e32 v3, 31, v2
	v_pk_fma_f32 v[6:7], v[52:53], s[50:51], v[166:167] op_sel_hi:[1,0,0]
	v_pk_fma_f32 v[4:5], v[50:51], s[50:51], v[166:167] op_sel_hi:[1,0,0]
	v_pk_fma_f32 v[10:11], v[44:45], s[50:51], v[166:167] op_sel_hi:[1,0,0]
	v_lshl_add_u64 v[8:9], v[8:9], 0, s[40:41]
	v_lshlrev_b64 v[2:3], 8, v[2:3]
	v_cvt_pk_bf16_f32 v4, v4, v5
	v_cvt_pk_bf16_f32 v5, v6, v7
	v_cvt_pk_bf16_f32 v6, v12, v13
	v_cvt_pk_bf16_f32 v7, v10, v11
	v_lshl_add_u64 v[8:9], v[8:9], 0, v[214:215]
	v_lshl_add_u64 v[2:3], s[10:11], 0, v[2:3]
	global_store_dwordx4 v[8:9], v[4:7], off
	v_pk_fma_f32 v[8:9], v[36:37], s[50:51], v[166:167] op_sel_hi:[1,0,0]
	v_pk_fma_f32 v[10:11], v[34:35], s[50:51], v[166:167] op_sel_hi:[1,0,0]
	v_pk_fma_f32 v[6:7], v[40:41], s[50:51], v[166:167] op_sel_hi:[1,0,0]
	v_pk_fma_f32 v[4:5], v[38:39], s[50:51], v[166:167] op_sel_hi:[1,0,0]
	v_lshl_add_u64 v[2:3], v[2:3], 0, s[40:41]
	v_cvt_pk_bf16_f32 v4, v4, v5
	v_cvt_pk_bf16_f32 v5, v6, v7
	v_cvt_pk_bf16_f32 v6, v10, v11
	v_cvt_pk_bf16_f32 v7, v8, v9
	v_lshl_add_u64 v[2:3], v[2:3], 0, v[214:215]
	s_andn2_b64 vcc, exec, s[18:19]
	s_mov_b64 s[18:19], -1
	global_store_dwordx4 v[2:3], v[4:7], off
	s_cbranch_vccnz .LBB0_264
	v_lshl_add_u32 v2, s76, 8, v183
	v_ashrrev_i32_e32 v3, 31, v2
	v_lshl_add_u64 v[2:3], v[2:3], 2, s[4:5]
	global_load_dword v180, v[2:3], off
	global_load_dword v178, v[2:3], off offset:64
	global_load_dword v176, v[2:3], off offset:128
	global_load_dword v174, v[2:3], off offset:192
	global_load_dword v172, v[2:3], off offset:512
	global_load_dword v170, v[2:3], off offset:576
	global_load_dword v168, v[2:3], off offset:640
	global_load_dword v166, v[2:3], off offset:704
	s_andn2_b64 vcc, exec, s[8:9]
	s_cbranch_vccnz .LBB0_263
	s_barrier
	s_branch .LBB0_263

.LBB0_1061:
	v_mov_b32_e32 v2, v243
	s_nop 15
	s_nop 15
	s_lshl_b32 s23, s51, 8
	v_readfirstlane_b32 s21, v2
	s_ashr_i32 s25, s21, 2
	s_andn2_b32 s25, s25, 63
	s_lshr_b32 s21, s21, 1
	s_add_i32 s25, s25, s23
	s_lshl_b32 s23, s76, 7
	s_and_b32 s21, s21, 0x60
	v_and_or_b32 v6, v2, 15, s25
	s_or_b32 s21, s21, s23
	v_lshrrev_b32_e32 v2, 1, v2
	v_and_or_b32 v4, v2, 24, s21
	s_waitcnt vmcnt(8)
	v_pk_fma_f32 v[2:3], v[210:211], s[50:51], v[78:79] op_sel_hi:[1,0,1]
	v_pk_fma_f32 v[16:17], v[206:207], s[50:51], v[82:83] op_sel_hi:[1,0,1]
	v_min_f32_e32 v2, 0x40e00000, v2
	v_mul_f32_e32 v8, 0xc01d265f, v2
	v_min_f32_e32 v3, 0x40e00000, v3
	v_exp_f32_e32 v10, v8
	v_mul_f32_e32 v8, 0xc01d265f, v3
	v_exp_f32_e32 v11, v8
	v_pk_fma_f32 v[8:9], v[212:213], s[50:51], v[80:81] op_sel_hi:[1,0,1]
	v_add_f32_e32 v10, 1.0, v10
	v_rcp_f32_e32 v10, v10
	v_add_f32_e32 v11, 1.0, v11
	v_rcp_f32_e32 v11, v11
	v_min_f32_e32 v8, 0x40e00000, v8
	v_min_f32_e32 v9, 0x40e00000, v9
	v_mul_f32_e32 v12, 0xc01d265f, v8
	v_mul_f32_e32 v13, 0xc01d265f, v9
	v_exp_f32_e32 v12, v12
	v_exp_f32_e32 v13, v13
	v_med3_f32 v16, v16, s71, v242
	v_med3_f32 v17, v17, s71, v242
	v_pk_fma_f32 v[14:15], v[208:209], s[50:51], v[84:85] op_sel_hi:[1,0,1]
	v_pk_add_f32 v[16:17], v[16:17], 1.0 op_sel_hi:[1,0]
	v_pk_mul_f32 v[2:3], v[2:3], v[10:11]
	v_med3_f32 v14, v14, s71, v242
	v_med3_f32 v15, v15, s71, v242
	v_pk_mul_f32 v[2:3], v[2:3], v[16:17]
	v_mov_b32_e32 v10, v215
	v_cvt_pk_fp8_f32 v10, v2, v3
	v_pk_add_f32 v[2:3], v[14:15], 1.0 op_sel_hi:[1,0]
	v_pk_fma_f32 v[14:15], v[202:203], s[50:51], v[70:71] op_sel_hi:[1,0,1]
	v_add_f32_e32 v12, 1.0, v12
	v_add_f32_e32 v13, 1.0, v13
	v_min_f32_e32 v14, 0x40e00000, v14
	v_rcp_f32_e32 v12, v12
	v_rcp_f32_e32 v13, v13
	v_min_f32_e32 v15, 0x40e00000, v15
	v_mul_f32_e32 v11, 0xc01d265f, v14
	v_exp_f32_e32 v11, v11
	v_mul_f32_e32 v16, 0xc01d265f, v15
	v_exp_f32_e32 v17, v16
	v_pk_mul_f32 v[8:9], v[8:9], v[12:13]
	v_pk_fma_f32 v[12:13], v[204:205], s[50:51], v[72:73] op_sel_hi:[1,0,1]
	v_add_f32_e32 v11, 1.0, v11
	v_min_f32_e32 v12, 0x40e00000, v12
	v_min_f32_e32 v13, 0x40e00000, v13
	v_rcp_f32_e32 v16, v11
	v_add_f32_e32 v11, 1.0, v17
	v_mul_f32_e32 v17, 0xc01d265f, v12
	v_exp_f32_e32 v18, v17
	v_mul_f32_e32 v17, 0xc01d265f, v13
	v_exp_f32_e32 v19, v17
	v_rcp_f32_e32 v17, v11
	v_pk_mul_f32 v[2:3], v[8:9], v[2:3]
	v_pk_fma_f32 v[8:9], v[198:199], s[50:51], v[74:75] op_sel_hi:[1,0,1]
	v_add_f32_e32 v11, 1.0, v18
	v_med3_f32 v8, v8, s71, v242
	v_med3_f32 v9, v9, s71, v242
	v_rcp_f32_e32 v18, v11
	v_add_f32_e32 v11, 1.0, v19
	v_pk_add_f32 v[8:9], v[8:9], 1.0 op_sel_hi:[1,0]
	v_rcp_f32_e32 v19, v11
	v_pk_mul_f32 v[14:15], v[14:15], v[16:17]
	v_mov_b32_e32 v11, v215
	v_pk_mul_f32 v[8:9], v[14:15], v[8:9]
	v_cvt_pk_fp8_f32 v10, v2, v3 op_sel:[0,0,1]
	v_pk_fma_f32 v[2:3], v[200:201], s[50:51], v[76:77] op_sel_hi:[1,0,1]
	v_cvt_pk_fp8_f32 v11, v8, v9
	v_med3_f32 v2, v2, s71, v242
	v_med3_f32 v3, v3, s71, v242
	v_pk_add_f32 v[2:3], v[2:3], 1.0 op_sel_hi:[1,0]
	v_pk_mul_f32 v[8:9], v[12:13], v[18:19]
	v_ashrrev_i32_e32 v7, 31, v6
	v_pk_mul_f32 v[2:3], v[8:9], v[2:3]
	v_ashrrev_i32_e32 v5, 31, v4
	v_cvt_pk_fp8_f32 v11, v2, v3 op_sel:[0,0,1]
	v_lshlrev_b64 v[2:3], 10, v[6:7]
	v_lshl_add_u64 v[2:3], s[14:15], 0, v[2:3]
	v_lshl_add_u64 v[2:3], v[2:3], 0, v[4:5]
	global_store_dwordx2 v[2:3], v[10:11], off
	v_pk_fma_f32 v[10:11], v[194:195], s[50:51], v[78:79] op_sel_hi:[1,0,1]
	v_pk_fma_f32 v[20:21], v[190:191], s[50:51], v[82:83] op_sel_hi:[1,0,1]
	v_min_f32_e32 v10, 0x40e00000, v10
	v_mul_f32_e32 v7, 0xc01d265f, v10
	v_min_f32_e32 v11, 0x40e00000, v11
	v_exp_f32_e32 v7, v7
	v_mul_f32_e32 v12, 0xc01d265f, v11
	v_exp_f32_e32 v15, v12
	v_pk_fma_f32 v[12:13], v[196:197], s[50:51], v[80:81] op_sel_hi:[1,0,1]
	v_add_f32_e32 v7, 1.0, v7
	v_min_f32_e32 v12, 0x40e00000, v12
	v_rcp_f32_e32 v14, v7
	v_add_f32_e32 v7, 1.0, v15
	v_mul_f32_e32 v15, 0xc01d265f, v12
	v_min_f32_e32 v13, 0x40e00000, v13
	v_exp_f32_e32 v16, v15
	v_mul_f32_e32 v15, 0xc01d265f, v13
	v_exp_f32_e32 v17, v15
	v_rcp_f32_e32 v15, v7
	v_med3_f32 v20, v20, s71, v242
	v_med3_f32 v21, v21, s71, v242
	v_pk_fma_f32 v[18:19], v[192:193], s[50:51], v[84:85] op_sel_hi:[1,0,1]
	v_pk_add_f32 v[20:21], v[20:21], 1.0 op_sel_hi:[1,0]
	v_pk_mul_f32 v[10:11], v[10:11], v[14:15]
	v_med3_f32 v18, v18, s71, v242
	v_med3_f32 v19, v19, s71, v242
	v_pk_mul_f32 v[10:11], v[10:11], v[20:21]
	v_mov_b32_e32 v14, v215
	v_add_f32_e32 v7, 1.0, v16
	v_cvt_pk_fp8_f32 v14, v10, v11
	v_pk_add_f32 v[10:11], v[18:19], 1.0 op_sel_hi:[1,0]
	v_pk_fma_f32 v[18:19], v[186:187], s[50:51], v[70:71] op_sel_hi:[1,0,1]
	v_rcp_f32_e32 v16, v7
	v_add_f32_e32 v7, 1.0, v17
	v_min_f32_e32 v18, 0x40e00000, v18
	v_rcp_f32_e32 v17, v7
	v_min_f32_e32 v19, 0x40e00000, v19
	v_mul_f32_e32 v7, 0xc01d265f, v18
	v_exp_f32_e32 v7, v7
	v_mul_f32_e32 v15, 0xc01d265f, v19
	v_exp_f32_e32 v15, v15
	v_pk_mul_f32 v[12:13], v[12:13], v[16:17]
	v_pk_fma_f32 v[16:17], v[188:189], s[50:51], v[72:73] op_sel_hi:[1,0,1]
	v_add_f32_e32 v7, 1.0, v7
	v_min_f32_e32 v16, 0x40e00000, v16
	v_min_f32_e32 v17, 0x40e00000, v17
	v_rcp_f32_e32 v20, v7
	v_add_f32_e32 v7, 1.0, v15
	v_mul_f32_e32 v15, 0xc01d265f, v16
	v_exp_f32_e32 v15, v15
	v_mul_f32_e32 v21, 0xc01d265f, v17
	v_exp_f32_e32 v23, v21
	v_rcp_f32_e32 v21, v7
	v_pk_mul_f32 v[10:11], v[12:13], v[10:11]
	v_pk_fma_f32 v[12:13], v[182:183], s[50:51], v[74:75] op_sel_hi:[1,0,1]
	v_add_f32_e32 v7, 1.0, v15
	v_med3_f32 v12, v12, s71, v242
	v_med3_f32 v13, v13, s71, v242
	v_rcp_f32_e32 v22, v7
	v_add_f32_e32 v7, 1.0, v23
	v_pk_add_f32 v[12:13], v[12:13], 1.0 op_sel_hi:[1,0]
	v_rcp_f32_e32 v23, v7
	v_pk_mul_f32 v[18:19], v[18:19], v[20:21]
	v_mov_b32_e32 v15, v215
	v_pk_mul_f32 v[12:13], v[18:19], v[12:13]
	v_cvt_pk_fp8_f32 v14, v10, v11 op_sel:[0,0,1]
	v_pk_fma_f32 v[10:11], v[184:185], s[50:51], v[76:77] op_sel_hi:[1,0,1]
	v_cvt_pk_fp8_f32 v15, v12, v13
	v_med3_f32 v10, v10, s71, v242
	v_med3_f32 v11, v11, s71, v242
	v_pk_add_f32 v[10:11], v[10:11], 1.0 op_sel_hi:[1,0]
	v_pk_mul_f32 v[12:13], v[16:17], v[22:23]
	v_or_b32_e32 v8, 16, v6
	v_pk_mul_f32 v[10:11], v[12:13], v[10:11]
	v_ashrrev_i32_e32 v9, 31, v8
	v_cvt_pk_fp8_f32 v15, v10, v11 op_sel:[0,0,1]
	v_pk_fma_f32 v[10:11], v[178:179], s[50:51], v[78:79] op_sel_hi:[1,0,1]
	v_lshlrev_b64 v[8:9], 10, v[8:9]
	v_min_f32_e32 v10, 0x40e00000, v10
	v_lshl_add_u64 v[8:9], s[14:15], 0, v[8:9]
	v_mul_f32_e32 v7, 0xc01d265f, v10
	v_min_f32_e32 v11, 0x40e00000, v11
	v_lshl_add_u64 v[8:9], v[8:9], 0, v[4:5]
	v_exp_f32_e32 v7, v7
	v_mul_f32_e32 v12, 0xc01d265f, v11
	global_store_dwordx2 v[8:9], v[14:15], off
	v_exp_f32_e32 v15, v12
	v_pk_fma_f32 v[12:13], v[180:181], s[50:51], v[80:81] op_sel_hi:[1,0,1]
	v_add_f32_e32 v7, 1.0, v7
	v_min_f32_e32 v12, 0x40e00000, v12
	v_rcp_f32_e32 v14, v7
	v_add_f32_e32 v7, 1.0, v15
	v_mul_f32_e32 v15, 0xc01d265f, v12
	v_min_f32_e32 v13, 0x40e00000, v13
	v_exp_f32_e32 v16, v15
	v_mul_f32_e32 v15, 0xc01d265f, v13
	v_exp_f32_e32 v17, v15
	v_rcp_f32_e32 v15, v7
	v_pk_fma_f32 v[20:21], v[174:175], s[50:51], v[82:83] op_sel_hi:[1,0,1]
	v_pk_fma_f32 v[18:19], v[176:177], s[50:51], v[84:85] op_sel_hi:[1,0,1]
	v_med3_f32 v20, v20, s71, v242
	v_med3_f32 v21, v21, s71, v242
	v_pk_add_f32 v[20:21], v[20:21], 1.0 op_sel_hi:[1,0]
	v_pk_mul_f32 v[10:11], v[10:11], v[14:15]
	v_med3_f32 v18, v18, s71, v242
	v_med3_f32 v19, v19, s71, v242
	v_pk_mul_f32 v[10:11], v[10:11], v[20:21]
	v_mov_b32_e32 v14, v215
	v_add_f32_e32 v7, 1.0, v16
	v_cvt_pk_fp8_f32 v14, v10, v11
	v_pk_add_f32 v[10:11], v[18:19], 1.0 op_sel_hi:[1,0]
	v_pk_fma_f32 v[18:19], v[170:171], s[50:51], v[70:71] op_sel_hi:[1,0,1]
	v_rcp_f32_e32 v16, v7
	v_add_f32_e32 v7, 1.0, v17
	v_min_f32_e32 v18, 0x40e00000, v18
	v_rcp_f32_e32 v17, v7
	v_min_f32_e32 v19, 0x40e00000, v19
	v_mul_f32_e32 v7, 0xc01d265f, v18
	v_exp_f32_e32 v7, v7
	v_mul_f32_e32 v15, 0xc01d265f, v19
	v_exp_f32_e32 v15, v15
	v_pk_mul_f32 v[12:13], v[12:13], v[16:17]
	v_pk_fma_f32 v[16:17], v[172:173], s[50:51], v[72:73] op_sel_hi:[1,0,1]
	v_add_f32_e32 v7, 1.0, v7
	v_min_f32_e32 v16, 0x40e00000, v16
	v_min_f32_e32 v17, 0x40e00000, v17
	v_rcp_f32_e32 v20, v7
	v_add_f32_e32 v7, 1.0, v15
	v_mul_f32_e32 v15, 0xc01d265f, v16
	v_exp_f32_e32 v15, v15
	v_mul_f32_e32 v21, 0xc01d265f, v17
	v_exp_f32_e32 v23, v21
	v_rcp_f32_e32 v21, v7
	v_pk_mul_f32 v[10:11], v[12:13], v[10:11]
	v_pk_fma_f32 v[12:13], v[166:167], s[50:51], v[74:75] op_sel_hi:[1,0,1]
	v_add_f32_e32 v7, 1.0, v15
	v_med3_f32 v12, v12, s71, v242
	v_med3_f32 v13, v13, s71, v242
	v_rcp_f32_e32 v22, v7
	v_add_f32_e32 v7, 1.0, v23
	v_pk_add_f32 v[12:13], v[12:13], 1.0 op_sel_hi:[1,0]
	v_rcp_f32_e32 v23, v7
	v_pk_mul_f32 v[18:19], v[18:19], v[20:21]
	v_mov_b32_e32 v15, v215
	v_pk_mul_f32 v[12:13], v[18:19], v[12:13]
	v_cvt_pk_fp8_f32 v14, v10, v11 op_sel:[0,0,1]
	v_pk_fma_f32 v[10:11], v[168:169], s[50:51], v[76:77] op_sel_hi:[1,0,1]
	v_cvt_pk_fp8_f32 v15, v12, v13
	v_med3_f32 v10, v10, s71, v242
	v_med3_f32 v11, v11, s71, v242
	v_pk_add_f32 v[10:11], v[10:11], 1.0 op_sel_hi:[1,0]
	v_pk_mul_f32 v[12:13], v[16:17], v[22:23]
	v_or_b32_e32 v8, 32, v6
	v_pk_mul_f32 v[10:11], v[12:13], v[10:11]
	v_ashrrev_i32_e32 v9, 31, v8
	v_cvt_pk_fp8_f32 v15, v10, v11 op_sel:[0,0,1]
	v_lshlrev_b64 v[8:9], 10, v[8:9]
	v_lshl_add_u64 v[8:9], s[14:15], 0, v[8:9]
	v_lshl_add_u64 v[8:9], v[8:9], 0, v[4:5]
	global_store_dwordx2 v[8:9], v[14:15], off
	v_pk_fma_f32 v[8:9], v[162:163], s[50:51], v[78:79] op_sel_hi:[1,0,1]
	v_pk_fma_f32 v[18:19], v[158:159], s[50:51], v[82:83] op_sel_hi:[1,0,1]
	v_min_f32_e32 v8, 0x40e00000, v8
	v_mul_f32_e32 v10, 0xc01d265f, v8
	v_min_f32_e32 v9, 0x40e00000, v9
	v_exp_f32_e32 v12, v10
	v_mul_f32_e32 v10, 0xc01d265f, v9
	v_exp_f32_e32 v13, v10
	v_pk_fma_f32 v[10:11], v[164:165], s[50:51], v[80:81] op_sel_hi:[1,0,1]
	v_add_f32_e32 v12, 1.0, v12
	v_rcp_f32_e32 v12, v12
	v_add_f32_e32 v13, 1.0, v13
	v_rcp_f32_e32 v13, v13
	v_min_f32_e32 v10, 0x40e00000, v10
	v_min_f32_e32 v11, 0x40e00000, v11
	v_mul_f32_e32 v14, 0xc01d265f, v10
	v_mul_f32_e32 v15, 0xc01d265f, v11
	v_exp_f32_e32 v14, v14
	v_exp_f32_e32 v15, v15
	v_med3_f32 v18, v18, s71, v242
	v_med3_f32 v19, v19, s71, v242
	v_pk_fma_f32 v[16:17], v[160:161], s[50:51], v[84:85] op_sel_hi:[1,0,1]
	v_pk_add_f32 v[18:19], v[18:19], 1.0 op_sel_hi:[1,0]
	v_pk_mul_f32 v[8:9], v[8:9], v[12:13]
	v_med3_f32 v16, v16, s71, v242
	v_med3_f32 v17, v17, s71, v242
	v_pk_mul_f32 v[8:9], v[8:9], v[18:19]
	v_mov_b32_e32 v12, v215
	v_cvt_pk_fp8_f32 v12, v8, v9
	v_pk_add_f32 v[8:9], v[16:17], 1.0 op_sel_hi:[1,0]
	v_pk_fma_f32 v[16:17], v[154:155], s[50:51], v[70:71] op_sel_hi:[1,0,1]
	v_add_f32_e32 v14, 1.0, v14
	v_add_f32_e32 v15, 1.0, v15
	v_min_f32_e32 v16, 0x40e00000, v16
	v_rcp_f32_e32 v14, v14
	v_rcp_f32_e32 v15, v15
	v_min_f32_e32 v17, 0x40e00000, v17
	v_mul_f32_e32 v13, 0xc01d265f, v16
	v_exp_f32_e32 v13, v13
	v_mul_f32_e32 v18, 0xc01d265f, v17
	v_exp_f32_e32 v19, v18
	v_pk_mul_f32 v[10:11], v[10:11], v[14:15]
	v_pk_fma_f32 v[14:15], v[156:157], s[50:51], v[72:73] op_sel_hi:[1,0,1]
	v_add_f32_e32 v13, 1.0, v13
	v_min_f32_e32 v14, 0x40e00000, v14
	v_min_f32_e32 v15, 0x40e00000, v15
	v_rcp_f32_e32 v18, v13
	v_add_f32_e32 v13, 1.0, v19
	v_mul_f32_e32 v19, 0xc01d265f, v14
	v_exp_f32_e32 v20, v19
	v_mul_f32_e32 v19, 0xc01d265f, v15
	v_exp_f32_e32 v21, v19
	v_rcp_f32_e32 v19, v13
	v_pk_mul_f32 v[8:9], v[10:11], v[8:9]
	v_pk_fma_f32 v[10:11], v[150:151], s[50:51], v[74:75] op_sel_hi:[1,0,1]
	v_add_f32_e32 v13, 1.0, v20
	v_med3_f32 v10, v10, s71, v242
	v_med3_f32 v11, v11, s71, v242
	v_rcp_f32_e32 v20, v13
	v_add_f32_e32 v13, 1.0, v21
	v_pk_add_f32 v[10:11], v[10:11], 1.0 op_sel_hi:[1,0]
	v_rcp_f32_e32 v21, v13
	v_pk_mul_f32 v[16:17], v[16:17], v[18:19]
	v_mov_b32_e32 v13, v215
	v_pk_mul_f32 v[10:11], v[16:17], v[10:11]
	v_cvt_pk_fp8_f32 v12, v8, v9 op_sel:[0,0,1]
	v_pk_fma_f32 v[8:9], v[152:153], s[50:51], v[76:77] op_sel_hi:[1,0,1]
	v_cvt_pk_fp8_f32 v13, v10, v11
	v_med3_f32 v8, v8, s71, v242
	v_med3_f32 v9, v9, s71, v242
	v_pk_add_f32 v[8:9], v[8:9], 1.0 op_sel_hi:[1,0]
	v_pk_mul_f32 v[10:11], v[14:15], v[20:21]
	v_or_b32_e32 v6, 48, v6
	v_pk_mul_f32 v[8:9], v[10:11], v[8:9]
	v_ashrrev_i32_e32 v7, 31, v6
	v_cvt_pk_fp8_f32 v13, v8, v9 op_sel:[0,0,1]
	v_lshlrev_b64 v[6:7], 10, v[6:7]
	v_lshl_add_u64 v[6:7], s[14:15], 0, v[6:7]
	v_lshl_add_u64 v[4:5], v[6:7], 0, v[4:5]
	global_store_dwordx2 v[4:5], v[12:13], off
	v_pk_fma_f32 v[4:5], v[146:147], s[50:51], v[78:79] op_sel_hi:[1,0,1]
	v_pk_fma_f32 v[14:15], v[142:143], s[50:51], v[82:83] op_sel_hi:[1,0,1]
	v_min_f32_e32 v4, 0x40e00000, v4
	v_mul_f32_e32 v6, 0xc01d265f, v4
	v_min_f32_e32 v5, 0x40e00000, v5
	v_exp_f32_e32 v8, v6
	v_mul_f32_e32 v6, 0xc01d265f, v5
	v_exp_f32_e32 v9, v6
	v_pk_fma_f32 v[6:7], v[148:149], s[50:51], v[80:81] op_sel_hi:[1,0,1]
	v_add_f32_e32 v8, 1.0, v8
	v_rcp_f32_e32 v8, v8
	v_add_f32_e32 v9, 1.0, v9
	v_rcp_f32_e32 v9, v9
	v_min_f32_e32 v6, 0x40e00000, v6
	v_min_f32_e32 v7, 0x40e00000, v7
	v_mul_f32_e32 v10, 0xc01d265f, v6
	v_mul_f32_e32 v11, 0xc01d265f, v7
	v_exp_f32_e32 v10, v10
	v_exp_f32_e32 v11, v11
	v_med3_f32 v14, v14, s71, v242
	v_med3_f32 v15, v15, s71, v242
	v_pk_fma_f32 v[12:13], v[144:145], s[50:51], v[84:85] op_sel_hi:[1,0,1]
	v_pk_add_f32 v[14:15], v[14:15], 1.0 op_sel_hi:[1,0]
	v_pk_mul_f32 v[4:5], v[4:5], v[8:9]
	v_med3_f32 v12, v12, s71, v242
	v_med3_f32 v13, v13, s71, v242
	v_pk_mul_f32 v[4:5], v[4:5], v[14:15]
	v_mov_b32_e32 v8, v215
	v_cvt_pk_fp8_f32 v8, v4, v5
	v_pk_add_f32 v[4:5], v[12:13], 1.0 op_sel_hi:[1,0]
	v_pk_fma_f32 v[12:13], v[138:139], s[50:51], v[70:71] op_sel_hi:[1,0,1]
	v_add_f32_e32 v10, 1.0, v10
	v_add_f32_e32 v11, 1.0, v11
	v_min_f32_e32 v12, 0x40e00000, v12
	v_rcp_f32_e32 v10, v10
	v_rcp_f32_e32 v11, v11
	v_min_f32_e32 v13, 0x40e00000, v13
	v_mul_f32_e32 v9, 0xc01d265f, v12
	v_exp_f32_e32 v9, v9
	v_mul_f32_e32 v14, 0xc01d265f, v13
	v_exp_f32_e32 v15, v14
	v_pk_mul_f32 v[6:7], v[6:7], v[10:11]
	v_pk_fma_f32 v[10:11], v[140:141], s[50:51], v[72:73] op_sel_hi:[1,0,1]
	v_add_f32_e32 v9, 1.0, v9
	v_min_f32_e32 v10, 0x40e00000, v10
	v_min_f32_e32 v11, 0x40e00000, v11
	v_rcp_f32_e32 v14, v9
	v_add_f32_e32 v9, 1.0, v15
	v_mul_f32_e32 v15, 0xc01d265f, v10
	v_exp_f32_e32 v16, v15
	v_mul_f32_e32 v15, 0xc01d265f, v11
	v_exp_f32_e32 v17, v15
	v_rcp_f32_e32 v15, v9
	v_pk_mul_f32 v[4:5], v[6:7], v[4:5]
	v_pk_fma_f32 v[6:7], v[134:135], s[50:51], v[74:75] op_sel_hi:[1,0,1]
	v_add_f32_e32 v9, 1.0, v16
	v_med3_f32 v6, v6, s71, v242
	v_med3_f32 v7, v7, s71, v242
	v_rcp_f32_e32 v16, v9
	v_add_f32_e32 v9, 1.0, v17
	v_pk_add_f32 v[6:7], v[6:7], 1.0 op_sel_hi:[1,0]
	v_rcp_f32_e32 v17, v9
	v_pk_mul_f32 v[12:13], v[12:13], v[14:15]
	v_mov_b32_e32 v9, v215
	v_pk_mul_f32 v[6:7], v[12:13], v[6:7]
	v_cvt_pk_fp8_f32 v8, v4, v5 op_sel:[0,0,1]
	v_pk_fma_f32 v[4:5], v[136:137], s[50:51], v[76:77] op_sel_hi:[1,0,1]
	v_cvt_pk_fp8_f32 v9, v6, v7
	v_med3_f32 v4, v4, s71, v242
	v_med3_f32 v5, v5, s71, v242
	v_pk_add_f32 v[4:5], v[4:5], 1.0 op_sel_hi:[1,0]
	v_pk_mul_f32 v[6:7], v[10:11], v[16:17]
	v_pk_fma_f32 v[14:15], v[126:127], s[50:51], v[82:83] op_sel_hi:[1,0,1]
	v_pk_mul_f32 v[4:5], v[6:7], v[4:5]
	v_med3_f32 v14, v14, s71, v242
	v_cvt_pk_fp8_f32 v9, v4, v5 op_sel:[0,0,1]
	v_add_co_u32_e32 v4, vcc, s2, v2
	v_med3_f32 v15, v15, s71, v242
	s_nop 0
	v_addc_co_u32_e32 v5, vcc, 0, v3, vcc
	global_store_dwordx2 v[4:5], v[8:9], off
	v_pk_fma_f32 v[4:5], v[130:131], s[50:51], v[78:79] op_sel_hi:[1,0,1]
	v_pk_fma_f32 v[12:13], v[128:129], s[50:51], v[84:85] op_sel_hi:[1,0,1]
	v_min_f32_e32 v4, 0x40e00000, v4
	v_mul_f32_e32 v6, 0xc01d265f, v4
	v_min_f32_e32 v5, 0x40e00000, v5
	v_exp_f32_e32 v8, v6
	v_mul_f32_e32 v6, 0xc01d265f, v5
	v_exp_f32_e32 v9, v6
	v_pk_fma_f32 v[6:7], v[132:133], s[50:51], v[80:81] op_sel_hi:[1,0,1]
	v_add_f32_e32 v8, 1.0, v8
	v_rcp_f32_e32 v8, v8
	v_add_f32_e32 v9, 1.0, v9
	v_rcp_f32_e32 v9, v9
	v_min_f32_e32 v6, 0x40e00000, v6
	v_min_f32_e32 v7, 0x40e00000, v7
	v_mul_f32_e32 v10, 0xc01d265f, v6
	v_mul_f32_e32 v11, 0xc01d265f, v7
	v_exp_f32_e32 v10, v10
	v_exp_f32_e32 v11, v11
	v_pk_add_f32 v[14:15], v[14:15], 1.0 op_sel_hi:[1,0]
	v_pk_mul_f32 v[4:5], v[4:5], v[8:9]
	v_med3_f32 v12, v12, s71, v242
	v_med3_f32 v13, v13, s71, v242
	v_pk_mul_f32 v[4:5], v[4:5], v[14:15]
	v_mov_b32_e32 v8, v215
	v_cvt_pk_fp8_f32 v8, v4, v5
	v_pk_add_f32 v[4:5], v[12:13], 1.0 op_sel_hi:[1,0]
	v_pk_fma_f32 v[12:13], v[122:123], s[50:51], v[70:71] op_sel_hi:[1,0,1]
	v_add_f32_e32 v10, 1.0, v10
	v_add_f32_e32 v11, 1.0, v11
	v_min_f32_e32 v12, 0x40e00000, v12
	v_rcp_f32_e32 v10, v10
	v_rcp_f32_e32 v11, v11
	v_min_f32_e32 v13, 0x40e00000, v13
	v_mul_f32_e32 v9, 0xc01d265f, v12
	v_exp_f32_e32 v9, v9
	v_mul_f32_e32 v14, 0xc01d265f, v13
	v_exp_f32_e32 v15, v14
	v_pk_mul_f32 v[6:7], v[6:7], v[10:11]
	v_pk_fma_f32 v[10:11], v[124:125], s[50:51], v[72:73] op_sel_hi:[1,0,1]
	v_add_f32_e32 v9, 1.0, v9
	v_min_f32_e32 v10, 0x40e00000, v10
	v_min_f32_e32 v11, 0x40e00000, v11
	v_rcp_f32_e32 v14, v9
	v_add_f32_e32 v9, 1.0, v15
	v_mul_f32_e32 v15, 0xc01d265f, v10
	v_exp_f32_e32 v16, v15
	v_mul_f32_e32 v15, 0xc01d265f, v11
	v_exp_f32_e32 v17, v15
	v_rcp_f32_e32 v15, v9
	v_pk_mul_f32 v[4:5], v[6:7], v[4:5]
	v_pk_fma_f32 v[6:7], v[118:119], s[50:51], v[74:75] op_sel_hi:[1,0,1]
	v_add_f32_e32 v9, 1.0, v16
	v_med3_f32 v6, v6, s71, v242
	v_med3_f32 v7, v7, s71, v242
	v_rcp_f32_e32 v16, v9
	v_add_f32_e32 v9, 1.0, v17
	v_pk_add_f32 v[6:7], v[6:7], 1.0 op_sel_hi:[1,0]
	v_rcp_f32_e32 v17, v9
	v_pk_mul_f32 v[12:13], v[12:13], v[14:15]
	v_mov_b32_e32 v9, v215
	v_pk_mul_f32 v[6:7], v[12:13], v[6:7]
	v_cvt_pk_fp8_f32 v8, v4, v5 op_sel:[0,0,1]
	v_pk_fma_f32 v[4:5], v[120:121], s[50:51], v[76:77] op_sel_hi:[1,0,1]
	v_cvt_pk_fp8_f32 v9, v6, v7
	v_med3_f32 v4, v4, s71, v242
	v_med3_f32 v5, v5, s71, v242
	v_pk_add_f32 v[4:5], v[4:5], 1.0 op_sel_hi:[1,0]
	v_pk_mul_f32 v[6:7], v[10:11], v[16:17]
	s_mov_b32 s21, 0x24000
	v_pk_mul_f32 v[4:5], v[6:7], v[4:5]
	v_pk_fma_f32 v[14:15], v[110:111], s[50:51], v[82:83] op_sel_hi:[1,0,1]
	v_cvt_pk_fp8_f32 v9, v4, v5 op_sel:[0,0,1]
	v_add_co_u32_e32 v4, vcc, s21, v2
	v_med3_f32 v14, v14, s71, v242
	s_nop 0
	v_addc_co_u32_e32 v5, vcc, 0, v3, vcc
	global_store_dwordx2 v[4:5], v[8:9], off
	v_pk_fma_f32 v[4:5], v[114:115], s[50:51], v[78:79] op_sel_hi:[1,0,1]
	v_med3_f32 v15, v15, s71, v242
	v_min_f32_e32 v4, 0x40e00000, v4
	v_mul_f32_e32 v6, 0xc01d265f, v4
	v_min_f32_e32 v5, 0x40e00000, v5
	v_exp_f32_e32 v8, v6
	v_mul_f32_e32 v6, 0xc01d265f, v5
	v_exp_f32_e32 v9, v6
	v_pk_fma_f32 v[6:7], v[116:117], s[50:51], v[80:81] op_sel_hi:[1,0,1]
	v_add_f32_e32 v8, 1.0, v8
	v_rcp_f32_e32 v8, v8
	v_add_f32_e32 v9, 1.0, v9
	v_rcp_f32_e32 v9, v9
	v_min_f32_e32 v6, 0x40e00000, v6
	v_min_f32_e32 v7, 0x40e00000, v7
	v_mul_f32_e32 v10, 0xc01d265f, v6
	v_mul_f32_e32 v11, 0xc01d265f, v7
	v_exp_f32_e32 v10, v10
	v_exp_f32_e32 v11, v11
	v_pk_fma_f32 v[12:13], v[112:113], s[50:51], v[84:85] op_sel_hi:[1,0,1]
	v_pk_add_f32 v[14:15], v[14:15], 1.0 op_sel_hi:[1,0]
	v_pk_mul_f32 v[4:5], v[4:5], v[8:9]
	v_med3_f32 v12, v12, s71, v242
	v_med3_f32 v13, v13, s71, v242
	v_pk_mul_f32 v[4:5], v[4:5], v[14:15]
	v_mov_b32_e32 v8, v215
	v_cvt_pk_fp8_f32 v8, v4, v5
	v_pk_add_f32 v[4:5], v[12:13], 1.0 op_sel_hi:[1,0]
	v_pk_fma_f32 v[12:13], v[106:107], s[50:51], v[70:71] op_sel_hi:[1,0,1]
	v_add_f32_e32 v10, 1.0, v10
	v_add_f32_e32 v11, 1.0, v11
	v_min_f32_e32 v12, 0x40e00000, v12
	v_rcp_f32_e32 v10, v10
	v_rcp_f32_e32 v11, v11
	v_min_f32_e32 v13, 0x40e00000, v13
	v_mul_f32_e32 v9, 0xc01d265f, v12
	v_exp_f32_e32 v9, v9
	v_mul_f32_e32 v14, 0xc01d265f, v13
	v_exp_f32_e32 v15, v14
	v_pk_mul_f32 v[6:7], v[6:7], v[10:11]
	v_pk_fma_f32 v[10:11], v[108:109], s[50:51], v[72:73] op_sel_hi:[1,0,1]
	v_add_f32_e32 v9, 1.0, v9
	v_min_f32_e32 v10, 0x40e00000, v10
	v_min_f32_e32 v11, 0x40e00000, v11
	v_rcp_f32_e32 v14, v9
	v_add_f32_e32 v9, 1.0, v15
	v_mul_f32_e32 v15, 0xc01d265f, v10
	v_exp_f32_e32 v16, v15
	v_mul_f32_e32 v15, 0xc01d265f, v11
	v_exp_f32_e32 v17, v15
	v_rcp_f32_e32 v15, v9
	v_pk_mul_f32 v[4:5], v[6:7], v[4:5]
	v_pk_fma_f32 v[6:7], v[102:103], s[50:51], v[74:75] op_sel_hi:[1,0,1]
	v_add_f32_e32 v9, 1.0, v16
	v_med3_f32 v6, v6, s71, v242
	v_med3_f32 v7, v7, s71, v242
	v_rcp_f32_e32 v16, v9
	v_add_f32_e32 v9, 1.0, v17
	v_pk_add_f32 v[6:7], v[6:7], 1.0 op_sel_hi:[1,0]
	v_rcp_f32_e32 v17, v9
	v_pk_mul_f32 v[12:13], v[12:13], v[14:15]
	v_mov_b32_e32 v9, v215
	v_pk_mul_f32 v[6:7], v[12:13], v[6:7]
	v_cvt_pk_fp8_f32 v8, v4, v5 op_sel:[0,0,1]
	v_pk_fma_f32 v[4:5], v[104:105], s[50:51], v[76:77] op_sel_hi:[1,0,1]
	v_cvt_pk_fp8_f32 v9, v6, v7
	v_med3_f32 v4, v4, s71, v242
	v_med3_f32 v5, v5, s71, v242
	v_pk_add_f32 v[4:5], v[4:5], 1.0 op_sel_hi:[1,0]
	v_pk_mul_f32 v[6:7], v[10:11], v[16:17]
	s_mov_b32 s21, 0x28000
	v_pk_mul_f32 v[4:5], v[6:7], v[4:5]
	v_pk_fma_f32 v[10:11], v[98:99], s[50:51], v[78:79] op_sel_hi:[1,0,1]
	v_cvt_pk_fp8_f32 v9, v4, v5 op_sel:[0,0,1]
	v_add_co_u32_e32 v4, vcc, s21, v2
	v_min_f32_e32 v10, 0x40e00000, v10
	v_min_f32_e32 v11, 0x40e00000, v11
	v_addc_co_u32_e32 v5, vcc, 0, v3, vcc
	v_mul_f32_e32 v12, 0xc01d265f, v10
	v_mul_f32_e32 v13, 0xc01d265f, v11
	global_store_dwordx2 v[4:5], v[8:9], off
	v_pk_fma_f32 v[8:9], v[100:101], s[50:51], v[80:81] op_sel_hi:[1,0,1]
	v_exp_f32_e32 v12, v12
	v_exp_f32_e32 v13, v13
	v_min_f32_e32 v8, 0x40e00000, v8
	v_min_f32_e32 v9, 0x40e00000, v9
	v_mul_f32_e32 v14, 0xc01d265f, v8
	v_mul_f32_e32 v15, 0xc01d265f, v9
	v_exp_f32_e32 v14, v14
	v_exp_f32_e32 v15, v15
	v_add_f32_e32 v12, 1.0, v12
	v_add_f32_e32 v13, 1.0, v13
	v_rcp_f32_e32 v12, v12
	v_rcp_f32_e32 v13, v13
	v_add_f32_e32 v14, 1.0, v14
	v_add_f32_e32 v15, 1.0, v15
	v_pk_fma_f32 v[6:7], v[94:95], s[50:51], v[82:83] op_sel_hi:[1,0,1]
	v_rcp_f32_e32 v14, v14
	v_rcp_f32_e32 v15, v15
	v_med3_f32 v6, v6, s71, v242
	v_med3_f32 v7, v7, s71, v242
	v_pk_mul_f32 v[10:11], v[10:11], v[12:13]
	v_pk_fma_f32 v[12:13], v[90:91], s[50:51], v[70:71] op_sel_hi:[1,0,1]
	v_pk_add_f32 v[6:7], v[6:7], 1.0 op_sel_hi:[1,0]
	v_min_f32_e32 v12, 0x40e00000, v12
	v_pk_mul_f32 v[6:7], v[10:11], v[6:7]
	v_mov_b32_e32 v10, v215
	v_min_f32_e32 v13, 0x40e00000, v13
	v_mul_f32_e32 v11, 0xc01d265f, v12
	v_cvt_pk_fp8_f32 v10, v6, v7
	v_pk_mul_f32 v[6:7], v[8:9], v[14:15]
	v_exp_f32_e32 v11, v11
	v_mul_f32_e32 v14, 0xc01d265f, v13
	v_exp_f32_e32 v15, v14
	v_pk_fma_f32 v[8:9], v[92:93], s[50:51], v[72:73] op_sel_hi:[1,0,1]
	v_add_f32_e32 v11, 1.0, v11
	v_min_f32_e32 v8, 0x40e00000, v8
	v_min_f32_e32 v9, 0x40e00000, v9
	v_rcp_f32_e32 v14, v11
	v_add_f32_e32 v11, 1.0, v15
	v_mul_f32_e32 v15, 0xc01d265f, v8
	v_exp_f32_e32 v16, v15
	v_mul_f32_e32 v15, 0xc01d265f, v9
	v_pk_fma_f32 v[4:5], v[96:97], s[50:51], v[84:85] op_sel_hi:[1,0,1]
	v_exp_f32_e32 v17, v15
	v_med3_f32 v4, v4, s71, v242
	v_med3_f32 v5, v5, s71, v242
	v_rcp_f32_e32 v15, v11
	v_pk_add_f32 v[4:5], v[4:5], 1.0 op_sel_hi:[1,0]
	v_add_f32_e32 v11, 1.0, v16
	v_pk_mul_f32 v[4:5], v[6:7], v[4:5]
	v_pk_fma_f32 v[6:7], v[86:87], s[50:51], v[74:75] op_sel_hi:[1,0,1]
	v_rcp_f32_e32 v16, v11
	v_med3_f32 v6, v6, s71, v242
	v_med3_f32 v7, v7, s71, v242
	v_add_f32_e32 v11, 1.0, v17
	v_pk_add_f32 v[6:7], v[6:7], 1.0 op_sel_hi:[1,0]
	v_rcp_f32_e32 v17, v11
	v_pk_mul_f32 v[12:13], v[12:13], v[14:15]
	v_mov_b32_e32 v11, v215
	v_pk_mul_f32 v[6:7], v[12:13], v[6:7]
	v_cvt_pk_fp8_f32 v10, v4, v5 op_sel:[0,0,1]
	v_pk_fma_f32 v[4:5], v[88:89], s[50:51], v[76:77] op_sel_hi:[1,0,1]
	v_cvt_pk_fp8_f32 v11, v6, v7
	v_med3_f32 v4, v4, s71, v242
	v_med3_f32 v5, v5, s71, v242
	v_pk_add_f32 v[4:5], v[4:5], 1.0 op_sel_hi:[1,0]
	v_pk_mul_f32 v[6:7], v[8:9], v[16:17]
	v_add_co_u32_e32 v2, vcc, 0x2c000, v2
	v_pk_mul_f32 v[4:5], v[6:7], v[4:5]
	s_nop 0
	v_addc_co_u32_e32 v3, vcc, 0, v3, vcc
	v_cvt_pk_fp8_f32 v11, v4, v5 op_sel:[0,0,1]
	s_and_b64 vcc, exec, s[4:5]
	s_mov_b64 s[4:5], -1
	global_store_dwordx2 v[2:3], v[10:11], off
	s_cbranch_vccnz .LBB0_1049
	s_ashr_i32 s21, s20, 31
	s_lshl_b64 s[4:5], s[20:21], 13
	s_add_u32 s21, s40, s4
	s_addc_u32 s23, s57, s5
	s_lshl_b32 s4, s24, 7
	s_ashr_i32 s5, s4, 31
	s_lshl_b64 s[4:5], s[4:5], 2
	s_add_u32 s4, s21, s4
	s_addc_u32 s5, s23, s5
	s_add_u32 s4, s4, s60
	s_addc_u32 s5, s5, 0
	v_mov_b32_e32 v221, v215
	v_lshl_add_u64 v[2:3], s[4:5], 0, v[220:221]
	s_mov_b64 s[78:79], 0x1000
	v_lshl_add_u64 v[4:5], v[2:3], 0, s[78:79]
	v_add_co_u32_e32 v2, vcc, 0x1000, v2
	global_load_dwordx4 v[70:73], v220, s[4:5] offset:16
	global_load_dwordx4 v[78:81], v220, s[4:5]
	v_addc_co_u32_e32 v3, vcc, 0, v3, vcc
	global_load_dwordx4 v[82:85], v[2:3], off
	global_load_dwordx4 v[74:77], v[4:5], off offset:16
	s_andn2_b64 vcc, exec, s[12:13]
	s_cbranch_vccnz .LBB0_1048
	s_barrier
	s_branch .LBB0_1048

.LBB0_1156:
	s_waitcnt vmcnt(8)
	v_pk_mul_f32 v[12:13], v[106:107], s[68:69] op_sel_hi:[1,0]
	v_pk_mul_f32 v[10:11], v[98:99], s[68:69] op_sel_hi:[1,0]
	v_mov_b32_e32 v16, v182
	s_nop 15
	s_nop 15
	v_pk_fma_f32 v[26:27], v[178:179], s[70:71], v[12:13] op_sel_hi:[1,0,1]
	v_readfirstlane_b32 s15, v16
	v_pk_fma_f32 v[30:31], v[174:175], s[70:71], v[10:11] op_sel_hi:[1,0,1]
	v_mov_b32_e32 v32, v215
	v_mov_b32_e32 v33, v215
	s_ashr_i32 s19, s15, 2
	v_cvt_pk_fp8_f32 v32, v26, v27
	v_cvt_pk_fp8_f32 v33, v30, v31
	s_lshl_b32 s17, s26, 8
	s_andn2_b32 s19, s19, 63
	v_pk_mul_f32 v[18:19], v[108:109], s[68:69] op_sel_hi:[1,0]
	v_pk_mul_f32 v[14:15], v[100:101], s[68:69] op_sel_hi:[1,0]
	s_add_i32 s19, s19, s17
	s_lshr_b32 s15, s15, 1
	v_and_or_b32 v22, v16, 15, s19
	s_lshl_b32 s17, s24, 8
	s_and_b32 s15, s15, 0x60
	v_pk_fma_f32 v[24:25], v[180:181], s[70:71], v[18:19] op_sel_hi:[1,0,1]
	v_pk_fma_f32 v[28:29], v[176:177], s[70:71], v[14:15] op_sel_hi:[1,0,1]
	s_or_b32 s15, s15, s17
	v_lshrrev_b32_e32 v16, 1, v16
	v_ashrrev_i32_e32 v23, 31, v22
	v_cvt_pk_fp8_f32 v32, v24, v25 op_sel:[0,0,1]
	v_cvt_pk_fp8_f32 v33, v28, v29 op_sel:[0,0,1]
	v_and_or_b32 v20, v16, 24, s15
	v_lshlrev_b64 v[16:17], 10, v[22:23]
	v_ashrrev_i32_e32 v21, 31, v20
	v_lshl_add_u64 v[16:17], s[10:11], 0, v[16:17]
	v_pk_mul_f32 v[4:5], v[102:103], s[68:69] op_sel_hi:[1,0]
	v_pk_mul_f32 v[2:3], v[94:95], s[68:69] op_sel_hi:[1,0]
	v_lshl_add_u64 v[16:17], v[16:17], 0, v[20:21]
	global_store_dwordx2 v[16:17], v[32:33], off
	v_pk_fma_f32 v[26:27], v[170:171], s[70:71], v[4:5] op_sel_hi:[1,0,1]
	v_pk_fma_f32 v[30:31], v[166:167], s[70:71], v[2:3] op_sel_hi:[1,0,1]
	v_mov_b32_e32 v32, v215
	v_mov_b32_e32 v33, v215
	v_cvt_pk_fp8_f32 v32, v26, v27
	v_cvt_pk_fp8_f32 v33, v30, v31
	v_pk_mul_f32 v[8:9], v[104:105], s[68:69] op_sel_hi:[1,0]
	v_pk_mul_f32 v[6:7], v[96:97], s[68:69] op_sel_hi:[1,0]
	v_pk_fma_f32 v[24:25], v[172:173], s[70:71], v[8:9] op_sel_hi:[1,0,1]
	v_pk_fma_f32 v[28:29], v[168:169], s[70:71], v[6:7] op_sel_hi:[1,0,1]
	v_cvt_pk_fp8_f32 v32, v24, v25 op_sel:[0,0,1]
	v_cvt_pk_fp8_f32 v33, v28, v29 op_sel:[0,0,1]
	v_pk_fma_f32 v[28:29], v[162:163], s[70:71], v[12:13] op_sel_hi:[1,0,1]
	v_mov_b32_e32 v94, v215
	v_mov_b32_e32 v95, v215
	global_store_dwordx2 v[16:17], v[32:33], off offset:128
	v_pk_fma_f32 v[32:33], v[158:159], s[70:71], v[10:11] op_sel_hi:[1,0,1]
	v_cvt_pk_fp8_f32 v94, v28, v29
	v_cvt_pk_fp8_f32 v95, v32, v33
	v_or_b32_e32 v24, 16, v22
	v_pk_fma_f32 v[26:27], v[164:165], s[70:71], v[18:19] op_sel_hi:[1,0,1]
	v_pk_fma_f32 v[30:31], v[160:161], s[70:71], v[14:15] op_sel_hi:[1,0,1]
	v_ashrrev_i32_e32 v25, 31, v24
	v_cvt_pk_fp8_f32 v94, v26, v27 op_sel:[0,0,1]
	v_cvt_pk_fp8_f32 v95, v30, v31 op_sel:[0,0,1]
	v_lshlrev_b64 v[24:25], 10, v[24:25]
	v_lshl_add_u64 v[24:25], s[10:11], 0, v[24:25]
	v_lshl_add_u64 v[24:25], v[24:25], 0, v[20:21]
	global_store_dwordx2 v[24:25], v[94:95], off
	v_pk_fma_f32 v[28:29], v[154:155], s[70:71], v[4:5] op_sel_hi:[1,0,1]
	v_pk_fma_f32 v[32:33], v[150:151], s[70:71], v[2:3] op_sel_hi:[1,0,1]
	v_mov_b32_e32 v94, v215
	v_mov_b32_e32 v95, v215
	v_cvt_pk_fp8_f32 v94, v28, v29
	v_cvt_pk_fp8_f32 v95, v32, v33
	v_pk_fma_f32 v[26:27], v[156:157], s[70:71], v[8:9] op_sel_hi:[1,0,1]
	v_pk_fma_f32 v[30:31], v[152:153], s[70:71], v[6:7] op_sel_hi:[1,0,1]
	v_cvt_pk_fp8_f32 v94, v26, v27 op_sel:[0,0,1]
	v_cvt_pk_fp8_f32 v95, v30, v31 op_sel:[0,0,1]
	v_pk_fma_f32 v[28:29], v[146:147], s[70:71], v[12:13] op_sel_hi:[1,0,1]
	v_pk_fma_f32 v[32:33], v[142:143], s[70:71], v[10:11] op_sel_hi:[1,0,1]
	v_pk_fma_f32 v[26:27], v[148:149], s[70:71], v[18:19] op_sel_hi:[1,0,1]
	global_store_dwordx2 v[24:25], v[94:95], off offset:128
	v_mov_b32_e32 v94, v215
	v_mov_b32_e32 v95, v215
	v_cvt_pk_fp8_f32 v94, v28, v29
	v_cvt_pk_fp8_f32 v95, v32, v33
	v_or_b32_e32 v24, 32, v22
	v_pk_fma_f32 v[30:31], v[144:145], s[70:71], v[14:15] op_sel_hi:[1,0,1]
	v_ashrrev_i32_e32 v25, 31, v24
	v_cvt_pk_fp8_f32 v94, v26, v27 op_sel:[0,0,1]
	v_cvt_pk_fp8_f32 v95, v30, v31 op_sel:[0,0,1]
	v_lshlrev_b64 v[24:25], 10, v[24:25]
	v_lshl_add_u64 v[24:25], s[10:11], 0, v[24:25]
	v_lshl_add_u64 v[24:25], v[24:25], 0, v[20:21]
	global_store_dwordx2 v[24:25], v[94:95], off
	v_pk_fma_f32 v[28:29], v[138:139], s[70:71], v[4:5] op_sel_hi:[1,0,1]
	v_pk_fma_f32 v[32:33], v[134:135], s[70:71], v[2:3] op_sel_hi:[1,0,1]
	v_mov_b32_e32 v94, v215
	v_mov_b32_e32 v95, v215
	v_cvt_pk_fp8_f32 v94, v28, v29
	v_cvt_pk_fp8_f32 v95, v32, v33
	v_pk_fma_f32 v[26:27], v[140:141], s[70:71], v[8:9] op_sel_hi:[1,0,1]
	v_pk_fma_f32 v[30:31], v[136:137], s[70:71], v[6:7] op_sel_hi:[1,0,1]
	v_cvt_pk_fp8_f32 v94, v26, v27 op_sel:[0,0,1]
	v_cvt_pk_fp8_f32 v95, v30, v31 op_sel:[0,0,1]
	v_or_b32_e32 v22, 48, v22
	v_pk_fma_f32 v[28:29], v[126:127], s[70:71], v[10:11] op_sel_hi:[1,0,1]
	v_mov_b32_e32 v30, v215
	global_store_dwordx2 v[24:25], v[94:95], off offset:128
	v_pk_fma_f32 v[24:25], v[130:131], s[70:71], v[12:13] op_sel_hi:[1,0,1]
	v_mov_b32_e32 v31, v215
	v_ashrrev_i32_e32 v23, 31, v22
	v_cvt_pk_fp8_f32 v30, v24, v25
	v_cvt_pk_fp8_f32 v31, v28, v29
	v_lshlrev_b64 v[22:23], 10, v[22:23]
	v_lshl_add_u64 v[22:23], s[10:11], 0, v[22:23]
	v_lshl_add_u64 v[20:21], v[22:23], 0, v[20:21]
	v_pk_fma_f32 v[22:23], v[132:133], s[70:71], v[18:19] op_sel_hi:[1,0,1]
	v_pk_fma_f32 v[26:27], v[128:129], s[70:71], v[14:15] op_sel_hi:[1,0,1]
	v_cvt_pk_fp8_f32 v30, v22, v23 op_sel:[0,0,1]
	v_cvt_pk_fp8_f32 v31, v26, v27 op_sel:[0,0,1]
	v_pk_fma_f32 v[24:25], v[122:123], s[70:71], v[4:5] op_sel_hi:[1,0,1]
	v_pk_fma_f32 v[28:29], v[118:119], s[70:71], v[2:3] op_sel_hi:[1,0,1]
	v_pk_fma_f32 v[22:23], v[124:125], s[70:71], v[8:9] op_sel_hi:[1,0,1]
	global_store_dwordx2 v[20:21], v[30:31], off
	v_mov_b32_e32 v30, v215
	v_mov_b32_e32 v31, v215
	v_cvt_pk_fp8_f32 v30, v24, v25
	v_cvt_pk_fp8_f32 v31, v28, v29
	v_pk_fma_f32 v[26:27], v[120:121], s[70:71], v[6:7] op_sel_hi:[1,0,1]
	v_pk_fma_f32 v[24:25], v[114:115], s[70:71], v[12:13] op_sel_hi:[1,0,1]
	v_cvt_pk_fp8_f32 v30, v22, v23 op_sel:[0,0,1]
	v_cvt_pk_fp8_f32 v31, v26, v27 op_sel:[0,0,1]
	v_pk_fma_f32 v[28:29], v[110:111], s[70:71], v[10:11] op_sel_hi:[1,0,1]
	v_pk_fma_f32 v[22:23], v[116:117], s[70:71], v[18:19] op_sel_hi:[1,0,1]
	v_pk_fma_f32 v[26:27], v[112:113], s[70:71], v[14:15] op_sel_hi:[1,0,1]
	global_store_dwordx2 v[20:21], v[30:31], off offset:128
	v_mov_b32_e32 v30, v215
	v_mov_b32_e32 v31, v215
	v_cvt_pk_fp8_f32 v30, v24, v25
	v_cvt_pk_fp8_f32 v31, v28, v29
	v_pk_fma_f32 v[24:25], v[90:91], s[70:71], v[4:5] op_sel_hi:[1,0,1]
	v_pk_fma_f32 v[28:29], v[86:87], s[70:71], v[2:3] op_sel_hi:[1,0,1]
	v_cvt_pk_fp8_f32 v30, v22, v23 op_sel:[0,0,1]
	v_cvt_pk_fp8_f32 v31, v26, v27 op_sel:[0,0,1]
	v_add_co_u32_e32 v22, vcc, s2, v16
	v_pk_fma_f32 v[26:27], v[88:89], s[70:71], v[6:7] op_sel_hi:[1,0,1]
	s_nop 0
	v_addc_co_u32_e32 v23, vcc, 0, v17, vcc
	global_store_dwordx2 v[22:23], v[30:31], off
	v_mov_b32_e32 v30, v215
	v_mov_b32_e32 v31, v215
	v_cvt_pk_fp8_f32 v30, v24, v25
	v_cvt_pk_fp8_f32 v31, v28, v29
	v_pk_fma_f32 v[22:23], v[92:93], s[70:71], v[8:9] op_sel_hi:[1,0,1]
	s_mov_b64 s[24:25], 0x20000
	v_cvt_pk_fp8_f32 v30, v22, v23 op_sel:[0,0,1]
	v_cvt_pk_fp8_f32 v31, v26, v27 op_sel:[0,0,1]
	v_lshl_add_u64 v[20:21], v[16:17], 0, s[24:25]
	v_pk_fma_f32 v[24:25], v[82:83], s[70:71], v[12:13] op_sel_hi:[1,0,1]
	v_pk_fma_f32 v[28:29], v[78:79], s[70:71], v[10:11] op_sel_hi:[1,0,1]
	global_store_dwordx2 v[20:21], v[30:31], off offset:128
	v_mov_b32_e32 v30, v215
	v_mov_b32_e32 v31, v215
	v_cvt_pk_fp8_f32 v30, v24, v25
	v_cvt_pk_fp8_f32 v31, v28, v29
	v_pk_fma_f32 v[22:23], v[84:85], s[70:71], v[18:19] op_sel_hi:[1,0,1]
	v_pk_fma_f32 v[26:27], v[80:81], s[70:71], v[14:15] op_sel_hi:[1,0,1]
	v_cvt_pk_fp8_f32 v30, v22, v23 op_sel:[0,0,1]
	v_cvt_pk_fp8_f32 v31, v26, v27 op_sel:[0,0,1]
	s_mov_b32 s15, 0x24000
	v_add_co_u32_e32 v22, vcc, s15, v16
	v_pk_fma_f32 v[24:25], v[74:75], s[70:71], v[4:5] op_sel_hi:[1,0,1]
	s_nop 0
	v_addc_co_u32_e32 v23, vcc, 0, v17, vcc
	global_store_dwordx2 v[22:23], v[30:31], off
	v_pk_fma_f32 v[28:29], v[70:71], s[70:71], v[2:3] op_sel_hi:[1,0,1]
	v_mov_b32_e32 v30, v215
	v_mov_b32_e32 v31, v215
	v_cvt_pk_fp8_f32 v30, v24, v25
	v_cvt_pk_fp8_f32 v31, v28, v29
	v_pk_fma_f32 v[22:23], v[76:77], s[70:71], v[8:9] op_sel_hi:[1,0,1]
	v_pk_fma_f32 v[26:27], v[72:73], s[70:71], v[6:7] op_sel_hi:[1,0,1]
	v_cvt_pk_fp8_f32 v30, v22, v23 op_sel:[0,0,1]
	v_cvt_pk_fp8_f32 v31, v26, v27 op_sel:[0,0,1]
	s_mov_b64 s[24:25], 0x24000
	v_lshl_add_u64 v[20:21], v[16:17], 0, s[24:25]
	v_pk_fma_f32 v[24:25], v[62:63], s[70:71], v[12:13] op_sel_hi:[1,0,1]
	global_store_dwordx2 v[20:21], v[30:31], off offset:128
	v_pk_fma_f32 v[28:29], v[58:59], s[70:71], v[10:11] op_sel_hi:[1,0,1]
	v_mov_b32_e32 v30, v215
	v_mov_b32_e32 v31, v215
	v_cvt_pk_fp8_f32 v30, v24, v25
	v_cvt_pk_fp8_f32 v31, v28, v29
	v_pk_fma_f32 v[22:23], v[64:65], s[70:71], v[18:19] op_sel_hi:[1,0,1]
	v_pk_fma_f32 v[26:27], v[60:61], s[70:71], v[14:15] op_sel_hi:[1,0,1]
	v_cvt_pk_fp8_f32 v30, v22, v23 op_sel:[0,0,1]
	v_cvt_pk_fp8_f32 v31, v26, v27 op_sel:[0,0,1]
	s_mov_b32 s15, 0x28000
	v_add_co_u32_e32 v22, vcc, s15, v16
	v_pk_fma_f32 v[24:25], v[54:55], s[70:71], v[4:5] op_sel_hi:[1,0,1]
	s_nop 0
	v_addc_co_u32_e32 v23, vcc, 0, v17, vcc
	global_store_dwordx2 v[22:23], v[30:31], off
	v_mov_b32_e32 v30, v215
	v_cvt_pk_fp8_f32 v30, v24, v25
	v_pk_fma_f32 v[22:23], v[56:57], s[70:71], v[8:9] op_sel_hi:[1,0,1]
	v_pk_fma_f32 v[12:13], v[46:47], s[70:71], v[12:13] op_sel_hi:[1,0,1]
	v_pk_fma_f32 v[10:11], v[42:43], s[70:71], v[10:11] op_sel_hi:[1,0,1]
	v_cvt_pk_fp8_f32 v30, v22, v23 op_sel:[0,0,1]
	v_mov_b32_e32 v22, v215
	v_mov_b32_e32 v23, v215
	v_cvt_pk_fp8_f32 v22, v12, v13
	v_cvt_pk_fp8_f32 v23, v10, v11
	v_pk_fma_f32 v[18:19], v[48:49], s[70:71], v[18:19] op_sel_hi:[1,0,1]
	v_pk_fma_f32 v[14:15], v[44:45], s[70:71], v[14:15] op_sel_hi:[1,0,1]
	v_cvt_pk_fp8_f32 v22, v18, v19 op_sel:[0,0,1]
	v_cvt_pk_fp8_f32 v23, v14, v15 op_sel:[0,0,1]
	s_mov_b32 s15, 0x2c000
	v_add_co_u32_e32 v10, vcc, s15, v16
	v_pk_fma_f32 v[28:29], v[50:51], s[70:71], v[2:3] op_sel_hi:[1,0,1]
	v_mov_b32_e32 v31, v215
	v_addc_co_u32_e32 v11, vcc, 0, v17, vcc
	v_cvt_pk_fp8_f32 v31, v28, v29
	global_store_dwordx2 v[10:11], v[22:23], off
	v_pk_fma_f32 v[4:5], v[38:39], s[70:71], v[4:5] op_sel_hi:[1,0,1]
	v_pk_fma_f32 v[2:3], v[34:35], s[70:71], v[2:3] op_sel_hi:[1,0,1]
	v_mov_b32_e32 v10, v215
	v_mov_b32_e32 v11, v215
	v_cvt_pk_fp8_f32 v10, v4, v5
	v_cvt_pk_fp8_f32 v11, v2, v3
	v_pk_fma_f32 v[26:27], v[52:53], s[70:71], v[6:7] op_sel_hi:[1,0,1]
	v_pk_fma_f32 v[8:9], v[40:41], s[70:71], v[8:9] op_sel_hi:[1,0,1]
	v_cvt_pk_fp8_f32 v31, v26, v27 op_sel:[0,0,1]
	v_pk_fma_f32 v[6:7], v[36:37], s[70:71], v[6:7] op_sel_hi:[1,0,1]
	v_cvt_pk_fp8_f32 v10, v8, v9 op_sel:[0,0,1]
	v_cvt_pk_fp8_f32 v11, v6, v7 op_sel:[0,0,1]
	s_mov_b64 s[24:25], 0x28000
	v_lshl_add_u64 v[20:21], v[16:17], 0, s[24:25]
	s_mov_b64 s[24:25], 0x2c000
	global_store_dwordx2 v[20:21], v[30:31], off offset:128
	v_lshl_add_u64 v[20:21], v[16:17], 0, s[24:25]
	s_mov_b64 s[24:25], -1
	s_and_b64 vcc, exec, s[4:5]
	global_store_dwordx2 v[20:21], v[10:11], off offset:128
	s_cbranch_vccnz .LBB0_1146
	s_ashr_i32 s15, s14, 31
	s_lshl_b64 s[4:5], s[14:15], 12
	s_add_u32 s15, s40, s4
	s_addc_u32 s17, s57, s5
	s_lshl_b32 s4, s18, 8
	s_ashr_i32 s5, s4, 31
	s_lshl_b64 s[4:5], s[4:5], 2
	s_add_u32 s4, s15, s4
	s_addc_u32 s5, s17, s5
	s_add_u32 s4, s4, s58
	s_addc_u32 s5, s5, 0
	global_load_dwordx4 v[98:101], v194, s[4:5] offset:16
	global_load_dwordx4 v[106:109], v194, s[4:5]
	global_load_dwordx4 v[94:97], v194, s[4:5] offset:528
	global_load_dwordx4 v[102:105], v194, s[4:5] offset:512
	s_andn2_b64 vcc, exec, s[8:9]
	s_cbranch_vccnz .LBB0_1145
	s_barrier
	s_branch .LBB0_1145
